# baseline (speedup 1.0000x reference)
.LBB8_27:
	s_add_u32 s40, s38, 0xfffd0080
	s_addc_u32 s41, s39, -1
	s_cmp_eq_u32 s87, 8
	s_cselect_b32 s43, s9, s41
	s_cselect_b32 s42, s8, s40
	s_cselect_b32 s41, s1, s86
	s_cselect_b32 s40, s0, s85
	s_add_i32 m0, s51, 0xc000
	ds_read_b128 v[136:139], v232
	ds_read_b128 v[148:151], v232 offset:1024
	ds_read_b128 v[152:155], v232 offset:2048
	ds_read_b128 v[156:159], v232 offset:3072
	ds_read_b128 v[160:163], v232 offset:4096
	ds_read_b128 v[164:167], v232 offset:5120
	ds_read_b128 v[168:171], v232 offset:6144
	ds_read_b128 v[172:175], v232 offset:7168
	global_load_lds_dwordx4 v184, s[38:39]
	s_add_i32 m0, s51, 0xe000
	s_nop 0
	global_load_lds_dwordx4 v186, s[38:39]
	s_waitcnt lgkmcnt(8)
	s_barrier
	s_waitcnt lgkmcnt(0)
	v_mfma_f32_16x16x32_f16 v[144:147], v[72:75], v[136:139], v[144:147]
	v_mfma_f32_16x16x32_f16 v[140:143], v[88:91], v[136:139], v[140:143]
	v_mfma_f32_16x16x32_f16 v[124:127], v[72:75], v[152:155], v[124:127]
	v_mfma_f32_16x16x32_f16 v[120:123], v[88:91], v[152:155], v[120:123]
	v_mfma_f32_16x16x32_f16 v[108:111], v[72:75], v[160:163], v[108:111]
	v_mfma_f32_16x16x32_f16 v[104:107], v[88:91], v[160:163], v[104:107]
	v_mfma_f32_16x16x32_f16 v[84:87], v[72:75], v[168:171], v[84:87]
	v_mfma_f32_16x16x32_f16 v[76:79], v[88:91], v[168:171], v[76:79]
	v_mfma_f32_16x16x32_f16 v[144:147], v[80:83], v[148:151], v[144:147]
	v_mfma_f32_16x16x32_f16 v[140:143], v[92:95], v[148:151], v[140:143]
	v_mfma_f32_16x16x32_f16 v[124:127], v[80:83], v[156:159], v[124:127]
	v_mfma_f32_16x16x32_f16 v[120:123], v[92:95], v[156:159], v[120:123]
	v_mfma_f32_16x16x32_f16 v[108:111], v[80:83], v[164:167], v[108:111]
	v_mfma_f32_16x16x32_f16 v[104:107], v[92:95], v[164:167], v[104:107]
	v_mfma_f32_16x16x32_f16 v[84:87], v[80:83], v[172:175], v[84:87]
	v_mfma_f32_16x16x32_f16 v[76:79], v[92:95], v[172:175], v[76:79]
	s_barrier
	s_add_i32 s88, s70, s50
	s_add_u32 s92, s40, 0x80
	s_addc_u32 s93, s41, 0
	s_mov_b32 m0, s88
	ds_read_b128 v[190:193], v233
	ds_read_b128 v[194:197], v233 offset:1024
	ds_read_b128 v[198:201], v233 offset:2048
	ds_read_b128 v[202:205], v233 offset:3072
	global_load_lds_dwordx4 v178, s[40:41]
	s_add_i32 m0, s88, 0x2000
	s_nop 0
	global_load_lds_dwordx4 v182, s[40:41]
	s_barrier
	s_waitcnt lgkmcnt(0)
	v_mfma_f32_16x16x32_f16 v[132:135], v[190:193], v[136:139], v[132:135]
	v_mfma_f32_16x16x32_f16 v[128:131], v[198:201], v[136:139], v[128:131]
	v_mfma_f32_16x16x32_f16 v[116:119], v[190:193], v[152:155], v[116:119]
	v_mfma_f32_16x16x32_f16 v[112:115], v[198:201], v[152:155], v[112:115]
	v_mfma_f32_16x16x32_f16 v[100:103], v[190:193], v[160:163], v[100:103]
	v_mfma_f32_16x16x32_f16 v[96:99], v[198:201], v[160:163], v[96:99]
	v_mfma_f32_16x16x32_f16 v[68:71], v[190:193], v[168:171], v[68:71]
	v_mfma_f32_16x16x32_f16 v[64:67], v[198:201], v[168:171], v[64:67]
	v_mfma_f32_16x16x32_f16 v[132:135], v[194:197], v[148:151], v[132:135]
	v_mfma_f32_16x16x32_f16 v[128:131], v[202:205], v[148:151], v[128:131]
	v_mfma_f32_16x16x32_f16 v[116:119], v[194:197], v[156:159], v[116:119]
	v_mfma_f32_16x16x32_f16 v[112:115], v[202:205], v[156:159], v[112:115]
	v_mfma_f32_16x16x32_f16 v[100:103], v[194:197], v[164:167], v[100:103]
	v_mfma_f32_16x16x32_f16 v[96:99], v[202:205], v[164:167], v[96:99]
	v_mfma_f32_16x16x32_f16 v[68:71], v[194:197], v[172:175], v[68:71]
	v_mfma_f32_16x16x32_f16 v[64:67], v[202:205], v[172:175], v[64:67]
	s_barrier
	s_mov_b32 m0, s51
	s_add_u32 s94, s42, 0x80
	s_addc_u32 s95, s43, 0
	ds_read_b128 v[136:139], v232 offset:16384
	ds_read_b128 v[148:151], v232 offset:17408
	ds_read_b128 v[152:155], v232 offset:18432
	ds_read_b128 v[156:159], v232 offset:19456
	ds_read_b128 v[160:163], v232 offset:20480
	ds_read_b128 v[164:167], v232 offset:21504
	ds_read_b128 v[168:171], v232 offset:22528
	ds_read_b128 v[172:175], v232 offset:23552
	global_load_lds_dwordx4 v176, s[42:43]
	s_mov_b32 m0, s52
	s_nop 0
	global_load_lds_dwordx4 v180, s[42:43]
	s_waitcnt vmcnt(10)
	s_barrier
	s_waitcnt lgkmcnt(0)
	v_mfma_f32_16x16x32_f16 v[60:63], v[72:75], v[136:139], v[60:63]
	v_mfma_f32_16x16x32_f16 v[56:59], v[88:91], v[136:139], v[56:59]
	v_mfma_f32_16x16x32_f16 v[44:47], v[72:75], v[152:155], v[44:47]
	v_mfma_f32_16x16x32_f16 v[40:43], v[88:91], v[152:155], v[40:43]
	v_mfma_f32_16x16x32_f16 v[28:31], v[72:75], v[160:163], v[28:31]
	v_mfma_f32_16x16x32_f16 v[24:27], v[88:91], v[160:163], v[24:27]
	v_mfma_f32_16x16x32_f16 v[12:15], v[72:75], v[168:171], v[12:15]
	v_mfma_f32_16x16x32_f16 v[8:11], v[88:91], v[168:171], v[8:11]
	v_mfma_f32_16x16x32_f16 v[60:63], v[80:83], v[148:151], v[60:63]
	v_mfma_f32_16x16x32_f16 v[56:59], v[92:95], v[148:151], v[56:59]
	v_mfma_f32_16x16x32_f16 v[44:47], v[80:83], v[156:159], v[44:47]
	v_mfma_f32_16x16x32_f16 v[40:43], v[92:95], v[156:159], v[40:43]
	v_mfma_f32_16x16x32_f16 v[28:31], v[80:83], v[164:167], v[28:31]
	v_mfma_f32_16x16x32_f16 v[24:27], v[92:95], v[164:167], v[24:27]
	v_mfma_f32_16x16x32_f16 v[12:15], v[80:83], v[172:175], v[12:15]
	v_mfma_f32_16x16x32_f16 v[8:11], v[92:95], v[172:175], v[8:11]
	s_barrier
	s_add_u32 s88, s40, 0xc000
	s_addc_u32 s89, s41, 0
	s_add_i32 s90, s71, s50
	s_mov_b32 m0, s90
	s_nop 0
	global_load_lds_dwordx4 v178, s[88:89]
	s_add_i32 m0, s90, 0x2000
	s_nop 0
	global_load_lds_dwordx4 v182, s[88:89]
	s_add_i32 s88, 0, 0x18000
	v_add_u32_e32 v92, s88, v228
	ds_read_b128 v[72:75], v92
	ds_read_b128 v[80:83], v92 offset:1024
	ds_read_b128 v[88:91], v92 offset:2048
	ds_read_b128 v[92:95], v92 offset:3072
	s_waitcnt vmcnt(6)
	s_barrier
	v_mfma_f32_16x16x32_f16 v[52:55], v[190:193], v[136:139], v[52:55]
	v_mfma_f32_16x16x32_f16 v[48:51], v[198:201], v[136:139], v[48:51]
	v_mfma_f32_16x16x32_f16 v[36:39], v[190:193], v[152:155], v[36:39]
	v_mfma_f32_16x16x32_f16 v[32:35], v[198:201], v[152:155], v[32:35]
	v_mfma_f32_16x16x32_f16 v[20:23], v[190:193], v[160:163], v[20:23]
	v_mfma_f32_16x16x32_f16 v[16:19], v[198:201], v[160:163], v[16:19]
	v_mfma_f32_16x16x32_f16 v[4:7], v[190:193], v[168:171], v[4:7]
	v_mfma_f32_16x16x32_f16 v[0:3], v[198:201], v[168:171], v[0:3]
	v_mfma_f32_16x16x32_f16 v[52:55], v[194:197], v[148:151], v[52:55]
	v_mfma_f32_16x16x32_f16 v[48:51], v[202:205], v[148:151], v[48:51]
	v_mfma_f32_16x16x32_f16 v[36:39], v[194:197], v[156:159], v[36:39]
	v_mfma_f32_16x16x32_f16 v[32:35], v[202:205], v[156:159], v[32:35]
	v_mfma_f32_16x16x32_f16 v[20:23], v[194:197], v[164:167], v[20:23]
	v_mfma_f32_16x16x32_f16 v[16:19], v[202:205], v[164:167], v[16:19]
	v_mfma_f32_16x16x32_f16 v[4:7], v[194:197], v[172:175], v[4:7]
	v_mfma_f32_16x16x32_f16 v[0:3], v[202:205], v[172:175], v[0:3]
	s_barrier
	s_add_u32 s42, s42, 0x30000
	s_addc_u32 s43, s43, 0
	s_mov_b32 m0, s53
	ds_read_b128 v[136:139], v232 offset:32768
	ds_read_b128 v[148:151], v232 offset:33792
	ds_read_b128 v[152:155], v232 offset:34816
	ds_read_b128 v[156:159], v232 offset:35840
	ds_read_b128 v[160:163], v232 offset:36864
	ds_read_b128 v[164:167], v232 offset:37888
	ds_read_b128 v[168:171], v232 offset:38912
	ds_read_b128 v[172:175], v232 offset:39936
	global_load_lds_dwordx4 v176, s[42:43]
	s_mov_b32 m0, s54
	s_nop 0
	global_load_lds_dwordx4 v180, s[42:43]
	s_waitcnt lgkmcnt(8)
	s_barrier
	s_waitcnt lgkmcnt(0)
	v_mfma_f32_16x16x32_f16 v[144:147], v[72:75], v[136:139], v[144:147]
	v_mfma_f32_16x16x32_f16 v[140:143], v[88:91], v[136:139], v[140:143]
	v_mfma_f32_16x16x32_f16 v[124:127], v[72:75], v[152:155], v[124:127]
	v_mfma_f32_16x16x32_f16 v[120:123], v[88:91], v[152:155], v[120:123]
	v_mfma_f32_16x16x32_f16 v[108:111], v[72:75], v[160:163], v[108:111]
	v_mfma_f32_16x16x32_f16 v[104:107], v[88:91], v[160:163], v[104:107]
	v_mfma_f32_16x16x32_f16 v[84:87], v[72:75], v[168:171], v[84:87]
	v_mfma_f32_16x16x32_f16 v[76:79], v[88:91], v[168:171], v[76:79]
	v_mfma_f32_16x16x32_f16 v[144:147], v[80:83], v[148:151], v[144:147]
	v_mfma_f32_16x16x32_f16 v[140:143], v[92:95], v[148:151], v[140:143]
	v_mfma_f32_16x16x32_f16 v[124:127], v[80:83], v[156:159], v[124:127]
	v_mfma_f32_16x16x32_f16 v[120:123], v[92:95], v[156:159], v[120:123]
	v_mfma_f32_16x16x32_f16 v[108:111], v[80:83], v[164:167], v[108:111]
	v_mfma_f32_16x16x32_f16 v[104:107], v[92:95], v[164:167], v[104:107]
	v_mfma_f32_16x16x32_f16 v[84:87], v[80:83], v[172:175], v[84:87]
	v_mfma_f32_16x16x32_f16 v[76:79], v[92:95], v[172:175], v[76:79]
	s_barrier
	s_add_i32 s42, 0, 0x1c000
	s_add_i32 s43, s88, s50
	v_add_u32_e32 v202, s42, v228
	s_mov_b32 m0, s43
	ds_read_b128 v[190:193], v202
	ds_read_b128 v[194:197], v202 offset:1024
	ds_read_b128 v[198:201], v202 offset:2048
	ds_read_b128 v[202:205], v202 offset:3072
	global_load_lds_dwordx4 v178, s[92:93]
	s_add_i32 m0, s43, 0x2000
	s_nop 0
	global_load_lds_dwordx4 v182, s[92:93]
	s_barrier
	s_waitcnt lgkmcnt(0)
	v_mfma_f32_16x16x32_f16 v[132:135], v[190:193], v[136:139], v[132:135]
	v_mfma_f32_16x16x32_f16 v[128:131], v[198:201], v[136:139], v[128:131]
	v_mfma_f32_16x16x32_f16 v[116:119], v[190:193], v[152:155], v[116:119]
	v_mfma_f32_16x16x32_f16 v[112:115], v[198:201], v[152:155], v[112:115]
	v_mfma_f32_16x16x32_f16 v[100:103], v[190:193], v[160:163], v[100:103]
	v_mfma_f32_16x16x32_f16 v[96:99], v[198:201], v[160:163], v[96:99]
	v_mfma_f32_16x16x32_f16 v[68:71], v[190:193], v[168:171], v[68:71]
	v_mfma_f32_16x16x32_f16 v[64:67], v[198:201], v[168:171], v[64:67]
	v_mfma_f32_16x16x32_f16 v[132:135], v[194:197], v[148:151], v[132:135]
	v_mfma_f32_16x16x32_f16 v[128:131], v[202:205], v[148:151], v[128:131]
	v_mfma_f32_16x16x32_f16 v[116:119], v[194:197], v[156:159], v[116:119]
	v_mfma_f32_16x16x32_f16 v[112:115], v[202:205], v[156:159], v[112:115]
	v_mfma_f32_16x16x32_f16 v[100:103], v[194:197], v[164:167], v[100:103]
	v_mfma_f32_16x16x32_f16 v[96:99], v[202:205], v[164:167], v[96:99]
	v_mfma_f32_16x16x32_f16 v[68:71], v[194:197], v[172:175], v[68:71]
	v_mfma_f32_16x16x32_f16 v[64:67], v[202:205], v[172:175], v[64:67]
	s_barrier
	s_mov_b32 m0, s59
	ds_read_b128 v[136:139], v232 offset:49152
	ds_read_b128 v[148:151], v232 offset:50176
	ds_read_b128 v[152:155], v232 offset:51200
	ds_read_b128 v[156:159], v232 offset:52224
	ds_read_b128 v[160:163], v232 offset:53248
	ds_read_b128 v[164:167], v232 offset:54272
	ds_read_b128 v[168:171], v232 offset:55296
	ds_read_b128 v[172:175], v232 offset:56320
	global_load_lds_dwordx4 v176, s[94:95]
	s_mov_b32 m0, s60
	s_nop 0
	global_load_lds_dwordx4 v180, s[94:95]
	s_waitcnt vmcnt(10)
	s_barrier
	s_waitcnt lgkmcnt(0)
	v_mfma_f32_16x16x32_f16 v[60:63], v[72:75], v[136:139], v[60:63]
	v_mfma_f32_16x16x32_f16 v[56:59], v[88:91], v[136:139], v[56:59]
	v_mfma_f32_16x16x32_f16 v[44:47], v[72:75], v[152:155], v[44:47]
	v_mfma_f32_16x16x32_f16 v[40:43], v[88:91], v[152:155], v[40:43]
	v_mfma_f32_16x16x32_f16 v[28:31], v[72:75], v[160:163], v[28:31]
	v_mfma_f32_16x16x32_f16 v[24:27], v[88:91], v[160:163], v[24:27]
	v_mfma_f32_16x16x32_f16 v[12:15], v[72:75], v[168:171], v[12:15]
	v_mfma_f32_16x16x32_f16 v[8:11], v[88:91], v[168:171], v[8:11]
	v_mfma_f32_16x16x32_f16 v[60:63], v[80:83], v[148:151], v[60:63]
	v_mfma_f32_16x16x32_f16 v[56:59], v[92:95], v[148:151], v[56:59]
	v_mfma_f32_16x16x32_f16 v[44:47], v[80:83], v[156:159], v[44:47]
	v_mfma_f32_16x16x32_f16 v[40:43], v[92:95], v[156:159], v[40:43]
	v_mfma_f32_16x16x32_f16 v[28:31], v[80:83], v[164:167], v[28:31]
	v_mfma_f32_16x16x32_f16 v[24:27], v[92:95], v[164:167], v[24:27]
	v_mfma_f32_16x16x32_f16 v[12:15], v[80:83], v[172:175], v[12:15]
	v_mfma_f32_16x16x32_f16 v[8:11], v[92:95], v[172:175], v[8:11]
	s_barrier
	s_add_u32 s40, s40, 0xc080
	s_addc_u32 s41, s41, 0
	s_add_i32 s42, s42, s50
	s_mov_b32 m0, s42
	s_nop 0
	global_load_lds_dwordx4 v178, s[40:41]
	s_add_i32 m0, s42, 0x2000
	s_nop 0
	global_load_lds_dwordx4 v182, s[40:41]
	ds_read_b128 v[72:75], v231
	ds_read_b128 v[80:83], v231 offset:1024
	ds_read_b128 v[88:91], v231 offset:2048
	ds_read_b128 v[92:95], v231 offset:3072
	s_waitcnt vmcnt(6)
	s_barrier
	v_mfma_f32_16x16x32_f16 v[52:55], v[190:193], v[136:139], v[52:55]
	v_mfma_f32_16x16x32_f16 v[48:51], v[198:201], v[136:139], v[48:51]
	v_mfma_f32_16x16x32_f16 v[36:39], v[190:193], v[152:155], v[36:39]
	v_mfma_f32_16x16x32_f16 v[32:35], v[198:201], v[152:155], v[32:35]
	v_mfma_f32_16x16x32_f16 v[20:23], v[190:193], v[160:163], v[20:23]
	v_mfma_f32_16x16x32_f16 v[16:19], v[198:201], v[160:163], v[16:19]
	v_mfma_f32_16x16x32_f16 v[4:7], v[190:193], v[168:171], v[4:7]
	v_mfma_f32_16x16x32_f16 v[0:3], v[198:201], v[168:171], v[0:3]
	v_mfma_f32_16x16x32_f16 v[52:55], v[194:197], v[148:151], v[52:55]
	v_mfma_f32_16x16x32_f16 v[48:51], v[202:205], v[148:151], v[48:51]
	v_mfma_f32_16x16x32_f16 v[36:39], v[194:197], v[156:159], v[36:39]
	v_mfma_f32_16x16x32_f16 v[32:35], v[202:205], v[156:159], v[32:35]
	v_mfma_f32_16x16x32_f16 v[20:23], v[194:197], v[164:167], v[20:23]
	v_mfma_f32_16x16x32_f16 v[16:19], v[202:205], v[164:167], v[16:19]
	v_mfma_f32_16x16x32_f16 v[4:7], v[194:197], v[172:175], v[4:7]
	v_mfma_f32_16x16x32_f16 v[0:3], v[202:205], v[172:175], v[0:3]
	s_barrier
	s_add_i32 s87, s87, 2
	s_add_u32 s38, s38, 0x100
	s_addc_u32 s39, s39, 0
	s_add_u32 s85, s85, 0x100
	s_addc_u32 s86, s86, 0
	s_cmp_gt_u32 s87, 9
	s_cbranch_scc0 .LBB8_27
	s_lshl_b32 s92, s84, 8
	s_add_i32 s92, s92, s58
	s_lshl_b32 s93, s83, 8
	s_or_b32 s93, s93, s61
	v_lshlrev_b32_e32 v237, 2, v226
	s_lshl_b32 s96, s93, 2
	s_add_u32 s94, s16, s96
	s_addc_u32 s95, s17, 0
	global_load_dwordx4 v[72:75], v237, s[94:95] offset:0
	global_load_dwordx4 v[80:83], v237, s[94:95] offset:16
	global_load_dwordx4 v[88:91], v237, s[94:95] offset:128
	global_load_dwordx4 v[92:95], v237, s[94:95] offset:144
	s_add_u32 s94, s18, s96
	s_addc_u32 s95, s19, 0
	global_load_dwordx4 v[136:139], v237, s[94:95] offset:0
	global_load_dwordx4 v[148:151], v237, s[94:95] offset:16
	global_load_dwordx4 v[152:155], v237, s[94:95] offset:128
	global_load_dwordx4 v[156:159], v237, s[94:95] offset:144
	s_add_u32 s94, s14, s96
	s_addc_u32 s95, s15, 0
	global_load_dwordx4 v[160:163], v237, s[94:95] offset:0
	global_load_dwordx4 v[164:167], v237, s[94:95] offset:16
	global_load_dwordx4 v[168:171], v237, s[94:95] offset:128
	global_load_dwordx4 v[172:175], v237, s[94:95] offset:144
	v_lshlrev_b32_e32 v190, 3, v227
	s_lshl_b32 s96, s92, 3
	s_add_u32 s94, s12, s96
	s_addc_u32 s95, s13, 0
	global_load_dwordx2 v[238:239], v190, s[94:95] offset:0
	global_load_dwordx2 v[192:193], v190, s[94:95] offset:128
	global_load_dwordx2 v[194:195], v190, s[94:95] offset:256
	global_load_dwordx2 v[196:197], v190, s[94:95] offset:384
	global_load_dwordx2 v[198:199], v190, s[94:95] offset:1024
	global_load_dwordx2 v[200:201], v190, s[94:95] offset:1152
	global_load_dwordx2 v[202:203], v190, s[94:95] offset:1280
	global_load_dwordx2 v[204:205], v190, s[94:95] offset:1408
	v_mul_u32_u24_e32 v191, 0x600, v227
	v_lshl_add_u32 v191, v226, 1, v191
	s_mul_i32 s96, s92, 0x600
	s_lshl_b32 s97, s93, 1
	s_add_u32 s96, s96, s97
	s_add_u32 s98, s10, s96
	s_addc_u32 s99, s11, 0
	s_add_u32 s94, s98, 0x0
	s_addc_u32 s95, s99, 0
	global_load_dwordx4 v[208:211], v191, s[94:95] offset:0 nt
	global_load_dwordx4 v[212:215], v191, s[94:95] offset:64 nt
	s_add_u32 s94, s98, 0x6000
	s_addc_u32 s95, s99, 0
	global_load_dwordx4 v[216:219], v191, s[94:95] offset:0 nt
	global_load_dwordx4 v[220:223], v191, s[94:95] offset:64 nt
	v_add_u32_e32 v224, s92, v229
	v_mul_u32_u24_e32 v224, 0x600, v224
	s_lshl_b32 s97, s93, 1
	v_add3_u32 v224, v224, v230, s97
	s_lshl_b32 s96, s83, 2
	s_lshr_b32 s97, s61, 6
	s_add_u32 s96, s96, s97
	s_lshl_b32 s96, s96, 19
	s_lshl_b32 s97, s92, 3
	s_add_u32 s96, s96, s97
	s_add_u32 s100, s28, s96
	s_addc_u32 s101, s29, 0
	s_waitcnt vmcnt(19)
	v_pk_add_f32 v[72:73], v[72:73], v[136:137]
	v_pk_add_f32 v[74:75], v[74:75], v[138:139]
	s_waitcnt vmcnt(18)
	v_pk_add_f32 v[80:81], v[80:81], v[148:149]
	v_pk_add_f32 v[82:83], v[82:83], v[150:151]
	s_waitcnt vmcnt(17)
	v_pk_add_f32 v[88:89], v[88:89], v[152:153]
	v_pk_add_f32 v[90:91], v[90:91], v[154:155]
	s_waitcnt vmcnt(16)
	v_pk_add_f32 v[92:93], v[92:93], v[156:157]
	v_pk_add_f32 v[94:95], v[94:95], v[158:159]
	v_pk_add_f32 v[144:145], v[144:145], v[72:73]
	v_pk_add_f32 v[146:147], v[146:147], v[74:75]
	v_pk_add_f32 v[124:125], v[124:125], v[72:73]
	v_pk_add_f32 v[126:127], v[126:127], v[74:75]
	v_pk_add_f32 v[108:109], v[108:109], v[72:73]
	v_pk_add_f32 v[110:111], v[110:111], v[74:75]
	v_pk_add_f32 v[84:85], v[84:85], v[72:73]
	v_pk_add_f32 v[86:87], v[86:87], v[74:75]
	v_pk_add_f32 v[60:61], v[60:61], v[72:73]
	v_pk_add_f32 v[62:63], v[62:63], v[74:75]
	v_pk_add_f32 v[44:45], v[44:45], v[72:73]
	v_pk_add_f32 v[46:47], v[46:47], v[74:75]
	v_pk_add_f32 v[28:29], v[28:29], v[72:73]
	v_pk_add_f32 v[30:31], v[30:31], v[74:75]
	v_pk_add_f32 v[12:13], v[12:13], v[72:73]
	v_pk_add_f32 v[14:15], v[14:15], v[74:75]
	v_pk_add_f32 v[140:141], v[140:141], v[80:81]
	v_pk_add_f32 v[142:143], v[142:143], v[82:83]
	v_pk_add_f32 v[120:121], v[120:121], v[80:81]
	v_pk_add_f32 v[122:123], v[122:123], v[82:83]
	v_pk_add_f32 v[104:105], v[104:105], v[80:81]
	v_pk_add_f32 v[106:107], v[106:107], v[82:83]
	v_pk_add_f32 v[76:77], v[76:77], v[80:81]
	v_pk_add_f32 v[78:79], v[78:79], v[82:83]
	v_pk_add_f32 v[56:57], v[56:57], v[80:81]
	v_pk_add_f32 v[58:59], v[58:59], v[82:83]
	v_pk_add_f32 v[40:41], v[40:41], v[80:81]
	v_pk_add_f32 v[42:43], v[42:43], v[82:83]
	v_pk_add_f32 v[24:25], v[24:25], v[80:81]
	v_pk_add_f32 v[26:27], v[26:27], v[82:83]
	v_pk_add_f32 v[8:9], v[8:9], v[80:81]
	v_pk_add_f32 v[10:11], v[10:11], v[82:83]
	v_pk_add_f32 v[132:133], v[132:133], v[88:89]
	v_pk_add_f32 v[134:135], v[134:135], v[90:91]
	v_pk_add_f32 v[116:117], v[116:117], v[88:89]
	v_pk_add_f32 v[118:119], v[118:119], v[90:91]
	v_pk_add_f32 v[100:101], v[100:101], v[88:89]
	v_pk_add_f32 v[102:103], v[102:103], v[90:91]
	v_pk_add_f32 v[68:69], v[68:69], v[88:89]
	v_pk_add_f32 v[70:71], v[70:71], v[90:91]
	v_pk_add_f32 v[52:53], v[52:53], v[88:89]
	v_pk_add_f32 v[54:55], v[54:55], v[90:91]
	v_pk_add_f32 v[36:37], v[36:37], v[88:89]
	v_pk_add_f32 v[38:39], v[38:39], v[90:91]
	v_pk_add_f32 v[20:21], v[20:21], v[88:89]
	v_pk_add_f32 v[22:23], v[22:23], v[90:91]
	v_pk_add_f32 v[4:5], v[4:5], v[88:89]
	v_pk_add_f32 v[6:7], v[6:7], v[90:91]
	v_pk_add_f32 v[128:129], v[128:129], v[92:93]
	v_pk_add_f32 v[130:131], v[130:131], v[94:95]
	v_pk_add_f32 v[112:113], v[112:113], v[92:93]
	v_pk_add_f32 v[114:115], v[114:115], v[94:95]
	v_pk_add_f32 v[96:97], v[96:97], v[92:93]
	v_pk_add_f32 v[98:99], v[98:99], v[94:95]
	v_pk_add_f32 v[64:65], v[64:65], v[92:93]
	v_pk_add_f32 v[66:67], v[66:67], v[94:95]
	v_pk_add_f32 v[48:49], v[48:49], v[92:93]
	v_pk_add_f32 v[50:51], v[50:51], v[94:95]
	v_pk_add_f32 v[32:33], v[32:33], v[92:93]
	v_pk_add_f32 v[34:35], v[34:35], v[94:95]
	v_pk_add_f32 v[16:17], v[16:17], v[92:93]
	v_pk_add_f32 v[18:19], v[18:19], v[94:95]
	v_pk_add_f32 v[0:1], v[0:1], v[92:93]
	v_pk_add_f32 v[2:3], v[2:3], v[94:95]
	s_add_u32 s94, s98, 0xc000
	s_addc_u32 s95, s99, 0
	global_load_dwordx4 v[240:243], v191, s[94:95] offset:0 nt
	global_load_dwordx4 v[244:247], v191, s[94:95] offset:64 nt
	s_add_u32 s94, s98, 0x12000
	s_addc_u32 s95, s99, 0
	global_load_dwordx4 v[248:251], v191, s[94:95] offset:0 nt
	global_load_dwordx4 v[252:255], v191, s[94:95] offset:64 nt
	s_add_u32 s94, s98, 0x30000
	s_addc_u32 s95, s99, 0
	global_load_dwordx4 v[136:139], v191, s[94:95] offset:0 nt
	global_load_dwordx4 v[148:151], v191, s[94:95] offset:64 nt
	s_add_u32 s94, s98, 0x36000
	s_addc_u32 s95, s99, 0
	global_load_dwordx4 v[152:155], v191, s[94:95] offset:0 nt
	global_load_dwordx4 v[156:159], v191, s[94:95] offset:64 nt
	s_waitcnt vmcnt(19)
	v_mul_f32_e64 v225, -v238, v239
	s_waitcnt vmcnt(11)
	v_fma_mix_f32 v72, v208, v239, v225 op_sel_hi:[1,0,0]
	v_fma_mix_f32 v73, v208, v239, v225 op_sel:[1,0,0] op_sel_hi:[1,0,0]
	v_fma_mix_f32 v74, v209, v239, v225 op_sel_hi:[1,0,0]
	v_fma_mix_f32 v75, v209, v239, v225 op_sel:[1,0,0] op_sel_hi:[1,0,0]
	v_fma_mix_f32 v80, v210, v239, v225 op_sel_hi:[1,0,0]
	v_fma_mix_f32 v81, v210, v239, v225 op_sel:[1,0,0] op_sel_hi:[1,0,0]
	v_fma_mix_f32 v82, v211, v239, v225 op_sel_hi:[1,0,0]
	v_fma_mix_f32 v83, v211, v239, v225 op_sel:[1,0,0] op_sel_hi:[1,0,0]
	v_pk_fma_f32 v[144:145], v[72:73], v[160:161], v[144:145]
	v_pk_fma_f32 v[146:147], v[74:75], v[162:163], v[146:147]
	v_pk_fma_f32 v[140:141], v[80:81], v[164:165], v[140:141]
	v_pk_fma_f32 v[142:143], v[82:83], v[166:167], v[142:143]
	v_cvt_pk_f16_f32 v144, v144, v145
	v_cvt_pk_f16_f32 v145, v146, v147
	v_cvt_pk_f16_f32 v146, v140, v141
	v_cvt_pk_f16_f32 v147, v142, v143
	ds_write_b128 v235, v[144:147]
	v_fma_mix_f32 v206, v144, 1.0, 0 op_sel_hi:[1,0,0]
	v_fma_mix_f32 v207, v144, v144, 0 op_sel_hi:[1,1,0]
	v_fma_mix_f32 v206, v144, 1.0, v206 op_sel:[1,0,0] op_sel_hi:[1,0,0]
	v_fma_mix_f32 v207, v144, v144, v207 op_sel:[1,1,0] op_sel_hi:[1,1,0]
	v_fma_mix_f32 v206, v145, 1.0, v206 op_sel_hi:[1,0,0]
	v_fma_mix_f32 v207, v145, v145, v207 op_sel_hi:[1,1,0]
	v_fma_mix_f32 v206, v145, 1.0, v206 op_sel:[1,0,0] op_sel_hi:[1,0,0]
	v_fma_mix_f32 v207, v145, v145, v207 op_sel:[1,1,0] op_sel_hi:[1,1,0]
	v_fma_mix_f32 v206, v146, 1.0, v206 op_sel_hi:[1,0,0]
	v_fma_mix_f32 v207, v146, v146, v207 op_sel_hi:[1,1,0]
	v_fma_mix_f32 v206, v146, 1.0, v206 op_sel:[1,0,0] op_sel_hi:[1,0,0]
	v_fma_mix_f32 v207, v146, v146, v207 op_sel:[1,1,0] op_sel_hi:[1,1,0]
	v_fma_mix_f32 v206, v147, 1.0, v206 op_sel_hi:[1,0,0]
	v_fma_mix_f32 v207, v147, v147, v207 op_sel_hi:[1,1,0]
	v_fma_mix_f32 v206, v147, 1.0, v206 op_sel:[1,0,0] op_sel_hi:[1,0,0]
	v_fma_mix_f32 v207, v147, v147, v207 op_sel:[1,1,0] op_sel_hi:[1,1,0]
	s_waitcnt vmcnt(10)
	v_fma_mix_f32 v72, v212, v239, v225 op_sel_hi:[1,0,0]
	v_fma_mix_f32 v73, v212, v239, v225 op_sel:[1,0,0] op_sel_hi:[1,0,0]
	v_fma_mix_f32 v74, v213, v239, v225 op_sel_hi:[1,0,0]
	v_fma_mix_f32 v75, v213, v239, v225 op_sel:[1,0,0] op_sel_hi:[1,0,0]
	v_fma_mix_f32 v80, v214, v239, v225 op_sel_hi:[1,0,0]
	v_fma_mix_f32 v81, v214, v239, v225 op_sel:[1,0,0] op_sel_hi:[1,0,0]
	v_fma_mix_f32 v82, v215, v239, v225 op_sel_hi:[1,0,0]
	v_fma_mix_f32 v83, v215, v239, v225 op_sel:[1,0,0] op_sel_hi:[1,0,0]
	v_pk_fma_f32 v[132:133], v[72:73], v[168:169], v[132:133]
	v_pk_fma_f32 v[134:135], v[74:75], v[170:171], v[134:135]
	v_pk_fma_f32 v[128:129], v[80:81], v[172:173], v[128:129]
	v_pk_fma_f32 v[130:131], v[82:83], v[174:175], v[130:131]
	v_cvt_pk_f16_f32 v132, v132, v133
	v_cvt_pk_f16_f32 v133, v134, v135
	v_cvt_pk_f16_f32 v134, v128, v129
	v_cvt_pk_f16_f32 v135, v130, v131
	ds_write_b128 v235, v[132:135] offset:64
	v_fma_mix_f32 v206, v132, 1.0, v206 op_sel_hi:[1,0,0]
	v_fma_mix_f32 v207, v132, v132, v207 op_sel_hi:[1,1,0]
	v_fma_mix_f32 v206, v132, 1.0, v206 op_sel:[1,0,0] op_sel_hi:[1,0,0]
	v_fma_mix_f32 v207, v132, v132, v207 op_sel:[1,1,0] op_sel_hi:[1,1,0]
	v_fma_mix_f32 v206, v133, 1.0, v206 op_sel_hi:[1,0,0]
	v_fma_mix_f32 v207, v133, v133, v207 op_sel_hi:[1,1,0]
	v_fma_mix_f32 v206, v133, 1.0, v206 op_sel:[1,0,0] op_sel_hi:[1,0,0]
	v_fma_mix_f32 v207, v133, v133, v207 op_sel:[1,1,0] op_sel_hi:[1,1,0]
	v_fma_mix_f32 v206, v134, 1.0, v206 op_sel_hi:[1,0,0]
	v_fma_mix_f32 v207, v134, v134, v207 op_sel_hi:[1,1,0]
	v_fma_mix_f32 v206, v134, 1.0, v206 op_sel:[1,0,0] op_sel_hi:[1,0,0]
	v_fma_mix_f32 v207, v134, v134, v207 op_sel:[1,1,0] op_sel_hi:[1,1,0]
	v_fma_mix_f32 v206, v135, 1.0, v206 op_sel_hi:[1,0,0]
	v_fma_mix_f32 v207, v135, v135, v207 op_sel_hi:[1,1,0]
	v_fma_mix_f32 v206, v135, 1.0, v206 op_sel:[1,0,0] op_sel_hi:[1,0,0]
	v_fma_mix_f32 v207, v135, v135, v207 op_sel:[1,1,0] op_sel_hi:[1,1,0]
	ds_read_b128 v[88:91], v236
	ds_read_b128 v[92:95], v236 offset:1152
	v_mul_f32_e64 v225, -v192, v193
	s_waitcnt vmcnt(9)
	v_fma_mix_f32 v72, v216, v193, v225 op_sel_hi:[1,0,0]
	v_fma_mix_f32 v73, v216, v193, v225 op_sel:[1,0,0] op_sel_hi:[1,0,0]
	v_fma_mix_f32 v74, v217, v193, v225 op_sel_hi:[1,0,0]
	v_fma_mix_f32 v75, v217, v193, v225 op_sel:[1,0,0] op_sel_hi:[1,0,0]
	v_fma_mix_f32 v80, v218, v193, v225 op_sel_hi:[1,0,0]
	v_fma_mix_f32 v81, v218, v193, v225 op_sel:[1,0,0] op_sel_hi:[1,0,0]
	v_fma_mix_f32 v82, v219, v193, v225 op_sel_hi:[1,0,0]
	v_fma_mix_f32 v83, v219, v193, v225 op_sel:[1,0,0] op_sel_hi:[1,0,0]
	v_pk_fma_f32 v[124:125], v[72:73], v[160:161], v[124:125]
	v_pk_fma_f32 v[126:127], v[74:75], v[162:163], v[126:127]
	v_pk_fma_f32 v[120:121], v[80:81], v[164:165], v[120:121]
	v_pk_fma_f32 v[122:123], v[82:83], v[166:167], v[122:123]
	v_cvt_pk_f16_f32 v124, v124, v125
	v_cvt_pk_f16_f32 v125, v126, v127
	v_cvt_pk_f16_f32 v126, v120, v121
	v_cvt_pk_f16_f32 v127, v122, v123
	s_waitcnt lgkmcnt(0)
	buffer_store_dwordx4 v[88:91], v224, s[24:27], 0 offen nt
	v_add_u32_e32 v82, 0x3000, v224
	buffer_store_dwordx4 v[92:95], v82, s[24:27], 0 offen nt
	ds_write_b128 v235, v[124:127]
	v_fma_mix_f32 v140, v124, 1.0, 0 op_sel_hi:[1,0,0]
	v_fma_mix_f32 v141, v124, v124, 0 op_sel_hi:[1,1,0]
	v_fma_mix_f32 v140, v124, 1.0, v140 op_sel:[1,0,0] op_sel_hi:[1,0,0]
	v_fma_mix_f32 v141, v124, v124, v141 op_sel:[1,1,0] op_sel_hi:[1,1,0]
	v_fma_mix_f32 v140, v125, 1.0, v140 op_sel_hi:[1,0,0]
	v_fma_mix_f32 v141, v125, v125, v141 op_sel_hi:[1,1,0]
	v_fma_mix_f32 v140, v125, 1.0, v140 op_sel:[1,0,0] op_sel_hi:[1,0,0]
	v_fma_mix_f32 v141, v125, v125, v141 op_sel:[1,1,0] op_sel_hi:[1,1,0]
	v_fma_mix_f32 v140, v126, 1.0, v140 op_sel_hi:[1,0,0]
	v_fma_mix_f32 v141, v126, v126, v141 op_sel_hi:[1,1,0]
	v_fma_mix_f32 v140, v126, 1.0, v140 op_sel:[1,0,0] op_sel_hi:[1,0,0]
	v_fma_mix_f32 v141, v126, v126, v141 op_sel:[1,1,0] op_sel_hi:[1,1,0]
	v_fma_mix_f32 v140, v127, 1.0, v140 op_sel_hi:[1,0,0]
	v_fma_mix_f32 v141, v127, v127, v141 op_sel_hi:[1,1,0]
	v_fma_mix_f32 v140, v127, 1.0, v140 op_sel:[1,0,0] op_sel_hi:[1,0,0]
	v_fma_mix_f32 v141, v127, v127, v141 op_sel:[1,1,0] op_sel_hi:[1,1,0]
	s_waitcnt vmcnt(10)
	v_fma_mix_f32 v72, v220, v193, v225 op_sel_hi:[1,0,0]
	v_fma_mix_f32 v73, v220, v193, v225 op_sel:[1,0,0] op_sel_hi:[1,0,0]
	v_fma_mix_f32 v74, v221, v193, v225 op_sel_hi:[1,0,0]
	v_fma_mix_f32 v75, v221, v193, v225 op_sel:[1,0,0] op_sel_hi:[1,0,0]
	v_fma_mix_f32 v80, v222, v193, v225 op_sel_hi:[1,0,0]
	v_fma_mix_f32 v81, v222, v193, v225 op_sel:[1,0,0] op_sel_hi:[1,0,0]
	v_fma_mix_f32 v82, v223, v193, v225 op_sel_hi:[1,0,0]
	v_fma_mix_f32 v83, v223, v193, v225 op_sel:[1,0,0] op_sel_hi:[1,0,0]
	v_pk_fma_f32 v[116:117], v[72:73], v[168:169], v[116:117]
	v_pk_fma_f32 v[118:119], v[74:75], v[170:171], v[118:119]
	v_pk_fma_f32 v[112:113], v[80:81], v[172:173], v[112:113]
	v_pk_fma_f32 v[114:115], v[82:83], v[174:175], v[114:115]
	v_cvt_pk_f16_f32 v116, v116, v117
	v_cvt_pk_f16_f32 v117, v118, v119
	v_cvt_pk_f16_f32 v118, v112, v113
	v_cvt_pk_f16_f32 v119, v114, v115
	ds_write_b128 v235, v[116:119] offset:64
	v_fma_mix_f32 v140, v116, 1.0, v140 op_sel_hi:[1,0,0]
	v_fma_mix_f32 v141, v116, v116, v141 op_sel_hi:[1,1,0]
	v_fma_mix_f32 v140, v116, 1.0, v140 op_sel:[1,0,0] op_sel_hi:[1,0,0]
	v_fma_mix_f32 v141, v116, v116, v141 op_sel:[1,1,0] op_sel_hi:[1,1,0]
	v_fma_mix_f32 v140, v117, 1.0, v140 op_sel_hi:[1,0,0]
	v_fma_mix_f32 v141, v117, v117, v141 op_sel_hi:[1,1,0]
	v_fma_mix_f32 v140, v117, 1.0, v140 op_sel:[1,0,0] op_sel_hi:[1,0,0]
	v_fma_mix_f32 v141, v117, v117, v141 op_sel:[1,1,0] op_sel_hi:[1,1,0]
	v_fma_mix_f32 v140, v118, 1.0, v140 op_sel_hi:[1,0,0]
	v_fma_mix_f32 v141, v118, v118, v141 op_sel_hi:[1,1,0]
	v_fma_mix_f32 v140, v118, 1.0, v140 op_sel:[1,0,0] op_sel_hi:[1,0,0]
	v_fma_mix_f32 v141, v118, v118, v141 op_sel:[1,1,0] op_sel_hi:[1,1,0]
	v_fma_mix_f32 v140, v119, 1.0, v140 op_sel_hi:[1,0,0]
	v_fma_mix_f32 v141, v119, v119, v141 op_sel_hi:[1,1,0]
	v_fma_mix_f32 v140, v119, 1.0, v140 op_sel:[1,0,0] op_sel_hi:[1,0,0]
	v_fma_mix_f32 v141, v119, v119, v141 op_sel:[1,1,0] op_sel_hi:[1,1,0]
	ds_read_b128 v[208:211], v236
	ds_read_b128 v[128:131], v236 offset:1152
	s_add_u32 s94, s98, 0x3c000
	s_addc_u32 s95, s99, 0
	global_load_dwordx4 v[212:215], v191, s[94:95] offset:0 nt
	global_load_dwordx4 v[144:147], v191, s[94:95] offset:64 nt
	s_add_u32 s94, s98, 0x42000
	s_addc_u32 s95, s99, 0
	global_load_dwordx4 v[132:135], v191, s[94:95] offset:0 nt
	global_load_dwordx4 v[88:91], v191, s[94:95] offset:64 nt
	v_mul_f32_e64 v225, -v194, v195
	s_waitcnt vmcnt(13)
	v_fma_mix_f32 v72, v240, v195, v225 op_sel_hi:[1,0,0]
	v_fma_mix_f32 v73, v240, v195, v225 op_sel:[1,0,0] op_sel_hi:[1,0,0]
	v_fma_mix_f32 v74, v241, v195, v225 op_sel_hi:[1,0,0]
	v_fma_mix_f32 v75, v241, v195, v225 op_sel:[1,0,0] op_sel_hi:[1,0,0]
	v_fma_mix_f32 v80, v242, v195, v225 op_sel_hi:[1,0,0]
	v_fma_mix_f32 v81, v242, v195, v225 op_sel:[1,0,0] op_sel_hi:[1,0,0]
	v_fma_mix_f32 v82, v243, v195, v225 op_sel_hi:[1,0,0]
	v_fma_mix_f32 v83, v243, v195, v225 op_sel:[1,0,0] op_sel_hi:[1,0,0]
	v_pk_fma_f32 v[108:109], v[72:73], v[160:161], v[108:109]
	v_pk_fma_f32 v[110:111], v[74:75], v[162:163], v[110:111]
	v_pk_fma_f32 v[104:105], v[80:81], v[164:165], v[104:105]
	v_pk_fma_f32 v[106:107], v[82:83], v[166:167], v[106:107]
	v_cvt_pk_f16_f32 v108, v108, v109
	v_cvt_pk_f16_f32 v109, v110, v111
	v_cvt_pk_f16_f32 v110, v104, v105
	v_cvt_pk_f16_f32 v111, v106, v107
	s_waitcnt lgkmcnt(0)
	v_add_u32_e32 v83, 0x6000, v224
	buffer_store_dwordx4 v[208:211], v83, s[24:27], 0 offen nt
	v_add_u32_e32 v82, 0x9000, v224
	buffer_store_dwordx4 v[128:131], v82, s[24:27], 0 offen nt
	ds_write_b128 v235, v[108:111]
	v_fma_mix_f32 v142, v108, 1.0, 0 op_sel_hi:[1,0,0]
	v_fma_mix_f32 v143, v108, v108, 0 op_sel_hi:[1,1,0]
	v_fma_mix_f32 v142, v108, 1.0, v142 op_sel:[1,0,0] op_sel_hi:[1,0,0]
	v_fma_mix_f32 v143, v108, v108, v143 op_sel:[1,1,0] op_sel_hi:[1,1,0]
	v_fma_mix_f32 v142, v109, 1.0, v142 op_sel_hi:[1,0,0]
	v_fma_mix_f32 v143, v109, v109, v143 op_sel_hi:[1,1,0]
	v_fma_mix_f32 v142, v109, 1.0, v142 op_sel:[1,0,0] op_sel_hi:[1,0,0]
	v_fma_mix_f32 v143, v109, v109, v143 op_sel:[1,1,0] op_sel_hi:[1,1,0]
	v_fma_mix_f32 v142, v110, 1.0, v142 op_sel_hi:[1,0,0]
	v_fma_mix_f32 v143, v110, v110, v143 op_sel_hi:[1,1,0]
	v_fma_mix_f32 v142, v110, 1.0, v142 op_sel:[1,0,0] op_sel_hi:[1,0,0]
	v_fma_mix_f32 v143, v110, v110, v143 op_sel:[1,1,0] op_sel_hi:[1,1,0]
	v_fma_mix_f32 v142, v111, 1.0, v142 op_sel_hi:[1,0,0]
	v_fma_mix_f32 v143, v111, v111, v143 op_sel_hi:[1,1,0]
	v_fma_mix_f32 v142, v111, 1.0, v142 op_sel:[1,0,0] op_sel_hi:[1,0,0]
	v_fma_mix_f32 v143, v111, v111, v143 op_sel:[1,1,0] op_sel_hi:[1,1,0]
	s_waitcnt vmcnt(14)
	v_fma_mix_f32 v72, v244, v195, v225 op_sel_hi:[1,0,0]
	v_fma_mix_f32 v73, v244, v195, v225 op_sel:[1,0,0] op_sel_hi:[1,0,0]
	v_fma_mix_f32 v74, v245, v195, v225 op_sel_hi:[1,0,0]
	v_fma_mix_f32 v75, v245, v195, v225 op_sel:[1,0,0] op_sel_hi:[1,0,0]
	v_fma_mix_f32 v80, v246, v195, v225 op_sel_hi:[1,0,0]
	v_fma_mix_f32 v81, v246, v195, v225 op_sel:[1,0,0] op_sel_hi:[1,0,0]
	v_fma_mix_f32 v82, v247, v195, v225 op_sel_hi:[1,0,0]
	v_fma_mix_f32 v83, v247, v195, v225 op_sel:[1,0,0] op_sel_hi:[1,0,0]
	v_pk_fma_f32 v[100:101], v[72:73], v[168:169], v[100:101]
	v_pk_fma_f32 v[102:103], v[74:75], v[170:171], v[102:103]
	v_pk_fma_f32 v[96:97], v[80:81], v[172:173], v[96:97]
	v_pk_fma_f32 v[98:99], v[82:83], v[174:175], v[98:99]
	v_cvt_pk_f16_f32 v100, v100, v101
	v_cvt_pk_f16_f32 v101, v102, v103
	v_cvt_pk_f16_f32 v102, v96, v97
	v_cvt_pk_f16_f32 v103, v98, v99
	ds_write_b128 v235, v[100:103] offset:64
	v_fma_mix_f32 v142, v100, 1.0, v142 op_sel_hi:[1,0,0]
	v_fma_mix_f32 v143, v100, v100, v143 op_sel_hi:[1,1,0]
	v_fma_mix_f32 v142, v100, 1.0, v142 op_sel:[1,0,0] op_sel_hi:[1,0,0]
	v_fma_mix_f32 v143, v100, v100, v143 op_sel:[1,1,0] op_sel_hi:[1,1,0]
	v_fma_mix_f32 v142, v101, 1.0, v142 op_sel_hi:[1,0,0]
	v_fma_mix_f32 v143, v101, v101, v143 op_sel_hi:[1,1,0]
	v_fma_mix_f32 v142, v101, 1.0, v142 op_sel:[1,0,0] op_sel_hi:[1,0,0]
	v_fma_mix_f32 v143, v101, v101, v143 op_sel:[1,1,0] op_sel_hi:[1,1,0]
	v_fma_mix_f32 v142, v102, 1.0, v142 op_sel_hi:[1,0,0]
	v_fma_mix_f32 v143, v102, v102, v143 op_sel_hi:[1,1,0]
	v_fma_mix_f32 v142, v102, 1.0, v142 op_sel:[1,0,0] op_sel_hi:[1,0,0]
	v_fma_mix_f32 v143, v102, v102, v143 op_sel:[1,1,0] op_sel_hi:[1,1,0]
	v_fma_mix_f32 v142, v103, 1.0, v142 op_sel_hi:[1,0,0]
	v_fma_mix_f32 v143, v103, v103, v143 op_sel_hi:[1,1,0]
	v_fma_mix_f32 v142, v103, 1.0, v142 op_sel:[1,0,0] op_sel_hi:[1,0,0]
	v_fma_mix_f32 v143, v103, v103, v143 op_sel:[1,1,0] op_sel_hi:[1,1,0]
	ds_read_b128 v[92:95], v236
	ds_read_b128 v[120:123], v236 offset:1152
	v_mul_f32_e64 v225, -v196, v197
	s_waitcnt vmcnt(13)
	v_fma_mix_f32 v72, v248, v197, v225 op_sel_hi:[1,0,0]
	v_fma_mix_f32 v73, v248, v197, v225 op_sel:[1,0,0] op_sel_hi:[1,0,0]
	v_fma_mix_f32 v74, v249, v197, v225 op_sel_hi:[1,0,0]
	v_fma_mix_f32 v75, v249, v197, v225 op_sel:[1,0,0] op_sel_hi:[1,0,0]
	v_fma_mix_f32 v80, v250, v197, v225 op_sel_hi:[1,0,0]
	v_fma_mix_f32 v81, v250, v197, v225 op_sel:[1,0,0] op_sel_hi:[1,0,0]
	v_fma_mix_f32 v82, v251, v197, v225 op_sel_hi:[1,0,0]
	v_fma_mix_f32 v83, v251, v197, v225 op_sel:[1,0,0] op_sel_hi:[1,0,0]
	v_pk_fma_f32 v[84:85], v[72:73], v[160:161], v[84:85]
	v_pk_fma_f32 v[86:87], v[74:75], v[162:163], v[86:87]
	v_pk_fma_f32 v[76:77], v[80:81], v[164:165], v[76:77]
	v_pk_fma_f32 v[78:79], v[82:83], v[166:167], v[78:79]
	v_cvt_pk_f16_f32 v84, v84, v85
	v_cvt_pk_f16_f32 v85, v86, v87
	v_cvt_pk_f16_f32 v86, v76, v77
	v_cvt_pk_f16_f32 v87, v78, v79
	s_waitcnt lgkmcnt(0)
	v_add_u32_e32 v83, 0xc000, v224
	buffer_store_dwordx4 v[92:95], v83, s[24:27], 0 offen nt
	v_add_u32_e32 v82, 0xf000, v224
	buffer_store_dwordx4 v[120:123], v82, s[24:27], 0 offen nt
	ds_write_b128 v235, v[84:87]
	v_fma_mix_f32 v216, v84, 1.0, 0 op_sel_hi:[1,0,0]
	v_fma_mix_f32 v217, v84, v84, 0 op_sel_hi:[1,1,0]
	v_fma_mix_f32 v216, v84, 1.0, v216 op_sel:[1,0,0] op_sel_hi:[1,0,0]
	v_fma_mix_f32 v217, v84, v84, v217 op_sel:[1,1,0] op_sel_hi:[1,1,0]
	v_fma_mix_f32 v216, v85, 1.0, v216 op_sel_hi:[1,0,0]
	v_fma_mix_f32 v217, v85, v85, v217 op_sel_hi:[1,1,0]
	v_fma_mix_f32 v216, v85, 1.0, v216 op_sel:[1,0,0] op_sel_hi:[1,0,0]
	v_fma_mix_f32 v217, v85, v85, v217 op_sel:[1,1,0] op_sel_hi:[1,1,0]
	v_fma_mix_f32 v216, v86, 1.0, v216 op_sel_hi:[1,0,0]
	v_fma_mix_f32 v217, v86, v86, v217 op_sel_hi:[1,1,0]
	v_fma_mix_f32 v216, v86, 1.0, v216 op_sel:[1,0,0] op_sel_hi:[1,0,0]
	v_fma_mix_f32 v217, v86, v86, v217 op_sel:[1,1,0] op_sel_hi:[1,1,0]
	v_fma_mix_f32 v216, v87, 1.0, v216 op_sel_hi:[1,0,0]
	v_fma_mix_f32 v217, v87, v87, v217 op_sel_hi:[1,1,0]
	v_fma_mix_f32 v216, v87, 1.0, v216 op_sel:[1,0,0] op_sel_hi:[1,0,0]
	v_fma_mix_f32 v217, v87, v87, v217 op_sel:[1,1,0] op_sel_hi:[1,1,0]
	s_waitcnt vmcnt(14)
	v_fma_mix_f32 v72, v252, v197, v225 op_sel_hi:[1,0,0]
	v_fma_mix_f32 v73, v252, v197, v225 op_sel:[1,0,0] op_sel_hi:[1,0,0]
	v_fma_mix_f32 v74, v253, v197, v225 op_sel_hi:[1,0,0]
	v_fma_mix_f32 v75, v253, v197, v225 op_sel:[1,0,0] op_sel_hi:[1,0,0]
	v_fma_mix_f32 v80, v254, v197, v225 op_sel_hi:[1,0,0]
	v_fma_mix_f32 v81, v254, v197, v225 op_sel:[1,0,0] op_sel_hi:[1,0,0]
	v_fma_mix_f32 v82, v255, v197, v225 op_sel_hi:[1,0,0]
	v_fma_mix_f32 v83, v255, v197, v225 op_sel:[1,0,0] op_sel_hi:[1,0,0]
	v_pk_fma_f32 v[68:69], v[72:73], v[168:169], v[68:69]
	v_pk_fma_f32 v[70:71], v[74:75], v[170:171], v[70:71]
	v_pk_fma_f32 v[64:65], v[80:81], v[172:173], v[64:65]
	v_pk_fma_f32 v[66:67], v[82:83], v[174:175], v[66:67]
	v_cvt_pk_f16_f32 v68, v68, v69
	v_cvt_pk_f16_f32 v69, v70, v71
	v_cvt_pk_f16_f32 v70, v64, v65
	v_cvt_pk_f16_f32 v71, v66, v67
	ds_write_b128 v235, v[68:71] offset:64
	v_fma_mix_f32 v216, v68, 1.0, v216 op_sel_hi:[1,0,0]
	v_fma_mix_f32 v217, v68, v68, v217 op_sel_hi:[1,1,0]
	v_fma_mix_f32 v216, v68, 1.0, v216 op_sel:[1,0,0] op_sel_hi:[1,0,0]
	v_fma_mix_f32 v217, v68, v68, v217 op_sel:[1,1,0] op_sel_hi:[1,1,0]
	v_fma_mix_f32 v216, v69, 1.0, v216 op_sel_hi:[1,0,0]
	v_fma_mix_f32 v217, v69, v69, v217 op_sel_hi:[1,1,0]
	v_fma_mix_f32 v216, v69, 1.0, v216 op_sel:[1,0,0] op_sel_hi:[1,0,0]
	v_fma_mix_f32 v217, v69, v69, v217 op_sel:[1,1,0] op_sel_hi:[1,1,0]
	v_fma_mix_f32 v216, v70, 1.0, v216 op_sel_hi:[1,0,0]
	v_fma_mix_f32 v217, v70, v70, v217 op_sel_hi:[1,1,0]
	v_fma_mix_f32 v216, v70, 1.0, v216 op_sel:[1,0,0] op_sel_hi:[1,0,0]
	v_fma_mix_f32 v217, v70, v70, v217 op_sel:[1,1,0] op_sel_hi:[1,1,0]
	v_fma_mix_f32 v216, v71, 1.0, v216 op_sel_hi:[1,0,0]
	v_fma_mix_f32 v217, v71, v71, v217 op_sel_hi:[1,1,0]
	v_fma_mix_f32 v216, v71, 1.0, v216 op_sel:[1,0,0] op_sel_hi:[1,0,0]
	v_fma_mix_f32 v217, v71, v71, v217 op_sel:[1,1,0] op_sel_hi:[1,1,0]
	ds_read_b128 v[112:115], v236
	ds_read_b128 v[220:223], v236 offset:1152
	v_mul_f32_e64 v225, -v198, v199
	s_waitcnt vmcnt(13)
	v_fma_mix_f32 v72, v136, v199, v225 op_sel_hi:[1,0,0]
	v_fma_mix_f32 v73, v136, v199, v225 op_sel:[1,0,0] op_sel_hi:[1,0,0]
	v_fma_mix_f32 v74, v137, v199, v225 op_sel_hi:[1,0,0]
	v_fma_mix_f32 v75, v137, v199, v225 op_sel:[1,0,0] op_sel_hi:[1,0,0]
	v_fma_mix_f32 v80, v138, v199, v225 op_sel_hi:[1,0,0]
	v_fma_mix_f32 v81, v138, v199, v225 op_sel:[1,0,0] op_sel_hi:[1,0,0]
	v_fma_mix_f32 v82, v139, v199, v225 op_sel_hi:[1,0,0]
	v_fma_mix_f32 v83, v139, v199, v225 op_sel:[1,0,0] op_sel_hi:[1,0,0]
	v_pk_fma_f32 v[60:61], v[72:73], v[160:161], v[60:61]
	v_pk_fma_f32 v[62:63], v[74:75], v[162:163], v[62:63]
	v_pk_fma_f32 v[56:57], v[80:81], v[164:165], v[56:57]
	v_pk_fma_f32 v[58:59], v[82:83], v[166:167], v[58:59]
	v_cvt_pk_f16_f32 v60, v60, v61
	v_cvt_pk_f16_f32 v61, v62, v63
	v_cvt_pk_f16_f32 v62, v56, v57
	v_cvt_pk_f16_f32 v63, v58, v59
	s_waitcnt lgkmcnt(0)
	v_add_u32_e32 v83, 0x12000, v224
	buffer_store_dwordx4 v[112:115], v83, s[24:27], 0 offen nt
	v_add_u32_e32 v82, 0x15000, v224
	buffer_store_dwordx4 v[220:223], v82, s[24:27], 0 offen nt
	ds_write_b128 v235, v[60:63]
	v_fma_mix_f32 v218, v60, 1.0, 0 op_sel_hi:[1,0,0]
	v_fma_mix_f32 v219, v60, v60, 0 op_sel_hi:[1,1,0]
	v_fma_mix_f32 v218, v60, 1.0, v218 op_sel:[1,0,0] op_sel_hi:[1,0,0]
	v_fma_mix_f32 v219, v60, v60, v219 op_sel:[1,1,0] op_sel_hi:[1,1,0]
	v_fma_mix_f32 v218, v61, 1.0, v218 op_sel_hi:[1,0,0]
	v_fma_mix_f32 v219, v61, v61, v219 op_sel_hi:[1,1,0]
	v_fma_mix_f32 v218, v61, 1.0, v218 op_sel:[1,0,0] op_sel_hi:[1,0,0]
	v_fma_mix_f32 v219, v61, v61, v219 op_sel:[1,1,0] op_sel_hi:[1,1,0]
	v_fma_mix_f32 v218, v62, 1.0, v218 op_sel_hi:[1,0,0]
	v_fma_mix_f32 v219, v62, v62, v219 op_sel_hi:[1,1,0]
	v_fma_mix_f32 v218, v62, 1.0, v218 op_sel:[1,0,0] op_sel_hi:[1,0,0]
	v_fma_mix_f32 v219, v62, v62, v219 op_sel:[1,1,0] op_sel_hi:[1,1,0]
	v_fma_mix_f32 v218, v63, 1.0, v218 op_sel_hi:[1,0,0]
	v_fma_mix_f32 v219, v63, v63, v219 op_sel_hi:[1,1,0]
	v_fma_mix_f32 v218, v63, 1.0, v218 op_sel:[1,0,0] op_sel_hi:[1,0,0]
	v_fma_mix_f32 v219, v63, v63, v219 op_sel:[1,1,0] op_sel_hi:[1,1,0]
	s_waitcnt vmcnt(14)
	v_fma_mix_f32 v72, v148, v199, v225 op_sel_hi:[1,0,0]
	v_fma_mix_f32 v73, v148, v199, v225 op_sel:[1,0,0] op_sel_hi:[1,0,0]
	v_fma_mix_f32 v74, v149, v199, v225 op_sel_hi:[1,0,0]
	v_fma_mix_f32 v75, v149, v199, v225 op_sel:[1,0,0] op_sel_hi:[1,0,0]
	v_fma_mix_f32 v80, v150, v199, v225 op_sel_hi:[1,0,0]
	v_fma_mix_f32 v81, v150, v199, v225 op_sel:[1,0,0] op_sel_hi:[1,0,0]
	v_fma_mix_f32 v82, v151, v199, v225 op_sel_hi:[1,0,0]
	v_fma_mix_f32 v83, v151, v199, v225 op_sel:[1,0,0] op_sel_hi:[1,0,0]
	v_pk_fma_f32 v[52:53], v[72:73], v[168:169], v[52:53]
	v_pk_fma_f32 v[54:55], v[74:75], v[170:171], v[54:55]
	v_pk_fma_f32 v[48:49], v[80:81], v[172:173], v[48:49]
	v_pk_fma_f32 v[50:51], v[82:83], v[174:175], v[50:51]
	v_cvt_pk_f16_f32 v52, v52, v53
	v_cvt_pk_f16_f32 v53, v54, v55
	v_cvt_pk_f16_f32 v54, v48, v49
	v_cvt_pk_f16_f32 v55, v50, v51
	ds_write_b128 v235, v[52:55] offset:64
	v_fma_mix_f32 v218, v52, 1.0, v218 op_sel_hi:[1,0,0]
	v_fma_mix_f32 v219, v52, v52, v219 op_sel_hi:[1,1,0]
	v_fma_mix_f32 v218, v52, 1.0, v218 op_sel:[1,0,0] op_sel_hi:[1,0,0]
	v_fma_mix_f32 v219, v52, v52, v219 op_sel:[1,1,0] op_sel_hi:[1,1,0]
	v_fma_mix_f32 v218, v53, 1.0, v218 op_sel_hi:[1,0,0]
	v_fma_mix_f32 v219, v53, v53, v219 op_sel_hi:[1,1,0]
	v_fma_mix_f32 v218, v53, 1.0, v218 op_sel:[1,0,0] op_sel_hi:[1,0,0]
	v_fma_mix_f32 v219, v53, v53, v219 op_sel:[1,1,0] op_sel_hi:[1,1,0]
	v_fma_mix_f32 v218, v54, 1.0, v218 op_sel_hi:[1,0,0]
	v_fma_mix_f32 v219, v54, v54, v219 op_sel_hi:[1,1,0]
	v_fma_mix_f32 v218, v54, 1.0, v218 op_sel:[1,0,0] op_sel_hi:[1,0,0]
	v_fma_mix_f32 v219, v54, v54, v219 op_sel:[1,1,0] op_sel_hi:[1,1,0]
	v_fma_mix_f32 v218, v55, 1.0, v218 op_sel_hi:[1,0,0]
	v_fma_mix_f32 v219, v55, v55, v219 op_sel_hi:[1,1,0]
	v_fma_mix_f32 v218, v55, 1.0, v218 op_sel:[1,0,0] op_sel_hi:[1,0,0]
	v_fma_mix_f32 v219, v55, v55, v219 op_sel:[1,1,0] op_sel_hi:[1,1,0]
	ds_read_b128 v[124:127], v236
	ds_read_b128 v[116:119], v236 offset:1152
	v_mul_f32_e64 v225, -v200, v201
	s_waitcnt vmcnt(13)
	v_fma_mix_f32 v72, v152, v201, v225 op_sel_hi:[1,0,0]
	v_fma_mix_f32 v73, v152, v201, v225 op_sel:[1,0,0] op_sel_hi:[1,0,0]
	v_fma_mix_f32 v74, v153, v201, v225 op_sel_hi:[1,0,0]
	v_fma_mix_f32 v75, v153, v201, v225 op_sel:[1,0,0] op_sel_hi:[1,0,0]
	v_fma_mix_f32 v80, v154, v201, v225 op_sel_hi:[1,0,0]
	v_fma_mix_f32 v81, v154, v201, v225 op_sel:[1,0,0] op_sel_hi:[1,0,0]
	v_fma_mix_f32 v82, v155, v201, v225 op_sel_hi:[1,0,0]
	v_fma_mix_f32 v83, v155, v201, v225 op_sel:[1,0,0] op_sel_hi:[1,0,0]
	v_pk_fma_f32 v[44:45], v[72:73], v[160:161], v[44:45]
	v_pk_fma_f32 v[46:47], v[74:75], v[162:163], v[46:47]
	v_pk_fma_f32 v[40:41], v[80:81], v[164:165], v[40:41]
	v_pk_fma_f32 v[42:43], v[82:83], v[166:167], v[42:43]
	v_cvt_pk_f16_f32 v44, v44, v45
	v_cvt_pk_f16_f32 v45, v46, v47
	v_cvt_pk_f16_f32 v46, v40, v41
	v_cvt_pk_f16_f32 v47, v42, v43
	s_waitcnt lgkmcnt(0)
	v_add_u32_e32 v83, 0x30000, v224
	buffer_store_dwordx4 v[124:127], v83, s[24:27], 0 offen nt
	v_add_u32_e32 v82, 0x33000, v224
	buffer_store_dwordx4 v[116:119], v82, s[24:27], 0 offen nt
	ds_write_b128 v235, v[44:47]
	v_fma_mix_f32 v208, v44, 1.0, 0 op_sel_hi:[1,0,0]
	v_fma_mix_f32 v209, v44, v44, 0 op_sel_hi:[1,1,0]
	v_fma_mix_f32 v208, v44, 1.0, v208 op_sel:[1,0,0] op_sel_hi:[1,0,0]
	v_fma_mix_f32 v209, v44, v44, v209 op_sel:[1,1,0] op_sel_hi:[1,1,0]
	v_fma_mix_f32 v208, v45, 1.0, v208 op_sel_hi:[1,0,0]
	v_fma_mix_f32 v209, v45, v45, v209 op_sel_hi:[1,1,0]
	v_fma_mix_f32 v208, v45, 1.0, v208 op_sel:[1,0,0] op_sel_hi:[1,0,0]
	v_fma_mix_f32 v209, v45, v45, v209 op_sel:[1,1,0] op_sel_hi:[1,1,0]
	v_fma_mix_f32 v208, v46, 1.0, v208 op_sel_hi:[1,0,0]
	v_fma_mix_f32 v209, v46, v46, v209 op_sel_hi:[1,1,0]
	v_fma_mix_f32 v208, v46, 1.0, v208 op_sel:[1,0,0] op_sel_hi:[1,0,0]
	v_fma_mix_f32 v209, v46, v46, v209 op_sel:[1,1,0] op_sel_hi:[1,1,0]
	v_fma_mix_f32 v208, v47, 1.0, v208 op_sel_hi:[1,0,0]
	v_fma_mix_f32 v209, v47, v47, v209 op_sel_hi:[1,1,0]
	v_fma_mix_f32 v208, v47, 1.0, v208 op_sel:[1,0,0] op_sel_hi:[1,0,0]
	v_fma_mix_f32 v209, v47, v47, v209 op_sel:[1,1,0] op_sel_hi:[1,1,0]
	s_waitcnt vmcnt(14)
	v_fma_mix_f32 v72, v156, v201, v225 op_sel_hi:[1,0,0]
	v_fma_mix_f32 v73, v156, v201, v225 op_sel:[1,0,0] op_sel_hi:[1,0,0]
	v_fma_mix_f32 v74, v157, v201, v225 op_sel_hi:[1,0,0]
	v_fma_mix_f32 v75, v157, v201, v225 op_sel:[1,0,0] op_sel_hi:[1,0,0]
	v_fma_mix_f32 v80, v158, v201, v225 op_sel_hi:[1,0,0]
	v_fma_mix_f32 v81, v158, v201, v225 op_sel:[1,0,0] op_sel_hi:[1,0,0]
	v_fma_mix_f32 v82, v159, v201, v225 op_sel_hi:[1,0,0]
	v_fma_mix_f32 v83, v159, v201, v225 op_sel:[1,0,0] op_sel_hi:[1,0,0]
	v_pk_fma_f32 v[36:37], v[72:73], v[168:169], v[36:37]
	v_pk_fma_f32 v[38:39], v[74:75], v[170:171], v[38:39]
	v_pk_fma_f32 v[32:33], v[80:81], v[172:173], v[32:33]
	v_pk_fma_f32 v[34:35], v[82:83], v[174:175], v[34:35]
	v_cvt_pk_f16_f32 v36, v36, v37
	v_cvt_pk_f16_f32 v37, v38, v39
	v_cvt_pk_f16_f32 v38, v32, v33
	v_cvt_pk_f16_f32 v39, v34, v35
	ds_write_b128 v235, v[36:39] offset:64
	v_fma_mix_f32 v208, v36, 1.0, v208 op_sel_hi:[1,0,0]
	v_fma_mix_f32 v209, v36, v36, v209 op_sel_hi:[1,1,0]
	v_fma_mix_f32 v208, v36, 1.0, v208 op_sel:[1,0,0] op_sel_hi:[1,0,0]
	v_fma_mix_f32 v209, v36, v36, v209 op_sel:[1,1,0] op_sel_hi:[1,1,0]
	v_fma_mix_f32 v208, v37, 1.0, v208 op_sel_hi:[1,0,0]
	v_fma_mix_f32 v209, v37, v37, v209 op_sel_hi:[1,1,0]
	v_fma_mix_f32 v208, v37, 1.0, v208 op_sel:[1,0,0] op_sel_hi:[1,0,0]
	v_fma_mix_f32 v209, v37, v37, v209 op_sel:[1,1,0] op_sel_hi:[1,1,0]
	v_fma_mix_f32 v208, v38, 1.0, v208 op_sel_hi:[1,0,0]
	v_fma_mix_f32 v209, v38, v38, v209 op_sel_hi:[1,1,0]
	v_fma_mix_f32 v208, v38, 1.0, v208 op_sel:[1,0,0] op_sel_hi:[1,0,0]
	v_fma_mix_f32 v209, v38, v38, v209 op_sel:[1,1,0] op_sel_hi:[1,1,0]
	v_fma_mix_f32 v208, v39, 1.0, v208 op_sel_hi:[1,0,0]
	v_fma_mix_f32 v209, v39, v39, v209 op_sel_hi:[1,1,0]
	v_fma_mix_f32 v208, v39, 1.0, v208 op_sel:[1,0,0] op_sel_hi:[1,0,0]
	v_fma_mix_f32 v209, v39, v39, v209 op_sel:[1,1,0] op_sel_hi:[1,1,0]
	ds_read_b128 v[128:131], v236
	ds_read_b128 v[104:107], v236 offset:1152
	v_mul_f32_e64 v225, -v202, v203
	s_waitcnt vmcnt(11)
	v_fma_mix_f32 v72, v212, v203, v225 op_sel_hi:[1,0,0]
	v_fma_mix_f32 v73, v212, v203, v225 op_sel:[1,0,0] op_sel_hi:[1,0,0]
	v_fma_mix_f32 v74, v213, v203, v225 op_sel_hi:[1,0,0]
	v_fma_mix_f32 v75, v213, v203, v225 op_sel:[1,0,0] op_sel_hi:[1,0,0]
	v_fma_mix_f32 v80, v214, v203, v225 op_sel_hi:[1,0,0]
	v_fma_mix_f32 v81, v214, v203, v225 op_sel:[1,0,0] op_sel_hi:[1,0,0]
	v_fma_mix_f32 v82, v215, v203, v225 op_sel_hi:[1,0,0]
	v_fma_mix_f32 v83, v215, v203, v225 op_sel:[1,0,0] op_sel_hi:[1,0,0]
	v_pk_fma_f32 v[28:29], v[72:73], v[160:161], v[28:29]
	v_pk_fma_f32 v[30:31], v[74:75], v[162:163], v[30:31]
	v_pk_fma_f32 v[24:25], v[80:81], v[164:165], v[24:25]
	v_pk_fma_f32 v[26:27], v[82:83], v[166:167], v[26:27]
	v_cvt_pk_f16_f32 v28, v28, v29
	v_cvt_pk_f16_f32 v29, v30, v31
	v_cvt_pk_f16_f32 v30, v24, v25
	v_cvt_pk_f16_f32 v31, v26, v27
	s_waitcnt lgkmcnt(0)
	v_add_u32_e32 v83, 0x36000, v224
	buffer_store_dwordx4 v[128:131], v83, s[24:27], 0 offen nt
	v_add_u32_e32 v82, 0x39000, v224
	buffer_store_dwordx4 v[104:107], v82, s[24:27], 0 offen nt
	ds_write_b128 v235, v[28:31]
	v_fma_mix_f32 v210, v28, 1.0, 0 op_sel_hi:[1,0,0]
	v_fma_mix_f32 v211, v28, v28, 0 op_sel_hi:[1,1,0]
	v_fma_mix_f32 v210, v28, 1.0, v210 op_sel:[1,0,0] op_sel_hi:[1,0,0]
	v_fma_mix_f32 v211, v28, v28, v211 op_sel:[1,1,0] op_sel_hi:[1,1,0]
	v_fma_mix_f32 v210, v29, 1.0, v210 op_sel_hi:[1,0,0]
	v_fma_mix_f32 v211, v29, v29, v211 op_sel_hi:[1,1,0]
	v_fma_mix_f32 v210, v29, 1.0, v210 op_sel:[1,0,0] op_sel_hi:[1,0,0]
	v_fma_mix_f32 v211, v29, v29, v211 op_sel:[1,1,0] op_sel_hi:[1,1,0]
	v_fma_mix_f32 v210, v30, 1.0, v210 op_sel_hi:[1,0,0]
	v_fma_mix_f32 v211, v30, v30, v211 op_sel_hi:[1,1,0]
	v_fma_mix_f32 v210, v30, 1.0, v210 op_sel:[1,0,0] op_sel_hi:[1,0,0]
	v_fma_mix_f32 v211, v30, v30, v211 op_sel:[1,1,0] op_sel_hi:[1,1,0]
	v_fma_mix_f32 v210, v31, 1.0, v210 op_sel_hi:[1,0,0]
	v_fma_mix_f32 v211, v31, v31, v211 op_sel_hi:[1,1,0]
	v_fma_mix_f32 v210, v31, 1.0, v210 op_sel:[1,0,0] op_sel_hi:[1,0,0]
	v_fma_mix_f32 v211, v31, v31, v211 op_sel:[1,1,0] op_sel_hi:[1,1,0]
	s_waitcnt vmcnt(12)
	v_fma_mix_f32 v72, v144, v203, v225 op_sel_hi:[1,0,0]
	v_fma_mix_f32 v73, v144, v203, v225 op_sel:[1,0,0] op_sel_hi:[1,0,0]
	v_fma_mix_f32 v74, v145, v203, v225 op_sel_hi:[1,0,0]
	v_fma_mix_f32 v75, v145, v203, v225 op_sel:[1,0,0] op_sel_hi:[1,0,0]
	v_fma_mix_f32 v80, v146, v203, v225 op_sel_hi:[1,0,0]
	v_fma_mix_f32 v81, v146, v203, v225 op_sel:[1,0,0] op_sel_hi:[1,0,0]
	v_fma_mix_f32 v82, v147, v203, v225 op_sel_hi:[1,0,0]
	v_fma_mix_f32 v83, v147, v203, v225 op_sel:[1,0,0] op_sel_hi:[1,0,0]
	v_pk_fma_f32 v[20:21], v[72:73], v[168:169], v[20:21]
	v_pk_fma_f32 v[22:23], v[74:75], v[170:171], v[22:23]
	v_pk_fma_f32 v[16:17], v[80:81], v[172:173], v[16:17]
	v_pk_fma_f32 v[18:19], v[82:83], v[174:175], v[18:19]
	v_cvt_pk_f16_f32 v20, v20, v21
	v_cvt_pk_f16_f32 v21, v22, v23
	v_cvt_pk_f16_f32 v22, v16, v17
	v_cvt_pk_f16_f32 v23, v18, v19
	ds_write_b128 v235, v[20:23] offset:64
	v_fma_mix_f32 v210, v20, 1.0, v210 op_sel_hi:[1,0,0]
	v_fma_mix_f32 v211, v20, v20, v211 op_sel_hi:[1,1,0]
	v_fma_mix_f32 v210, v20, 1.0, v210 op_sel:[1,0,0] op_sel_hi:[1,0,0]
	v_fma_mix_f32 v211, v20, v20, v211 op_sel:[1,1,0] op_sel_hi:[1,1,0]
	v_fma_mix_f32 v210, v21, 1.0, v210 op_sel_hi:[1,0,0]
	v_fma_mix_f32 v211, v21, v21, v211 op_sel_hi:[1,1,0]
	v_fma_mix_f32 v210, v21, 1.0, v210 op_sel:[1,0,0] op_sel_hi:[1,0,0]
	v_fma_mix_f32 v211, v21, v21, v211 op_sel:[1,1,0] op_sel_hi:[1,1,0]
	v_fma_mix_f32 v210, v22, 1.0, v210 op_sel_hi:[1,0,0]
	v_fma_mix_f32 v211, v22, v22, v211 op_sel_hi:[1,1,0]
	v_fma_mix_f32 v210, v22, 1.0, v210 op_sel:[1,0,0] op_sel_hi:[1,0,0]
	v_fma_mix_f32 v211, v22, v22, v211 op_sel:[1,1,0] op_sel_hi:[1,1,0]
	v_fma_mix_f32 v210, v23, 1.0, v210 op_sel_hi:[1,0,0]
	v_fma_mix_f32 v211, v23, v23, v211 op_sel_hi:[1,1,0]
	v_fma_mix_f32 v210, v23, 1.0, v210 op_sel:[1,0,0] op_sel_hi:[1,0,0]
	v_fma_mix_f32 v211, v23, v23, v211 op_sel:[1,1,0] op_sel_hi:[1,1,0]
	ds_read_b128 v[240:243], v236
	ds_read_b128 v[96:99], v236 offset:1152
	v_mul_f32_e64 v225, -v204, v205
	s_waitcnt vmcnt(11)
	v_fma_mix_f32 v72, v132, v205, v225 op_sel_hi:[1,0,0]
	v_fma_mix_f32 v73, v132, v205, v225 op_sel:[1,0,0] op_sel_hi:[1,0,0]
	v_fma_mix_f32 v74, v133, v205, v225 op_sel_hi:[1,0,0]
	v_fma_mix_f32 v75, v133, v205, v225 op_sel:[1,0,0] op_sel_hi:[1,0,0]
	v_fma_mix_f32 v80, v134, v205, v225 op_sel_hi:[1,0,0]
	v_fma_mix_f32 v81, v134, v205, v225 op_sel:[1,0,0] op_sel_hi:[1,0,0]
	v_fma_mix_f32 v82, v135, v205, v225 op_sel_hi:[1,0,0]
	v_fma_mix_f32 v83, v135, v205, v225 op_sel:[1,0,0] op_sel_hi:[1,0,0]
	v_pk_fma_f32 v[12:13], v[72:73], v[160:161], v[12:13]
	v_pk_fma_f32 v[14:15], v[74:75], v[162:163], v[14:15]
	v_pk_fma_f32 v[8:9], v[80:81], v[164:165], v[8:9]
	v_pk_fma_f32 v[10:11], v[82:83], v[166:167], v[10:11]
	v_cvt_pk_f16_f32 v12, v12, v13
	v_cvt_pk_f16_f32 v13, v14, v15
	v_cvt_pk_f16_f32 v14, v8, v9
	v_cvt_pk_f16_f32 v15, v10, v11
	s_waitcnt lgkmcnt(0)
	v_add_u32_e32 v83, 0x3c000, v224
	buffer_store_dwordx4 v[240:243], v83, s[24:27], 0 offen nt
	v_add_u32_e32 v82, 0x3f000, v224
	buffer_store_dwordx4 v[96:99], v82, s[24:27], 0 offen nt
	ds_write_b128 v235, v[12:15]
	v_fma_mix_f32 v244, v12, 1.0, 0 op_sel_hi:[1,0,0]
	v_fma_mix_f32 v245, v12, v12, 0 op_sel_hi:[1,1,0]
	v_fma_mix_f32 v244, v12, 1.0, v244 op_sel:[1,0,0] op_sel_hi:[1,0,0]
	v_fma_mix_f32 v245, v12, v12, v245 op_sel:[1,1,0] op_sel_hi:[1,1,0]
	v_fma_mix_f32 v244, v13, 1.0, v244 op_sel_hi:[1,0,0]
	v_fma_mix_f32 v245, v13, v13, v245 op_sel_hi:[1,1,0]
	v_fma_mix_f32 v244, v13, 1.0, v244 op_sel:[1,0,0] op_sel_hi:[1,0,0]
	v_fma_mix_f32 v245, v13, v13, v245 op_sel:[1,1,0] op_sel_hi:[1,1,0]
	v_fma_mix_f32 v244, v14, 1.0, v244 op_sel_hi:[1,0,0]
	v_fma_mix_f32 v245, v14, v14, v245 op_sel_hi:[1,1,0]
	v_fma_mix_f32 v244, v14, 1.0, v244 op_sel:[1,0,0] op_sel_hi:[1,0,0]
	v_fma_mix_f32 v245, v14, v14, v245 op_sel:[1,1,0] op_sel_hi:[1,1,0]
	v_fma_mix_f32 v244, v15, 1.0, v244 op_sel_hi:[1,0,0]
	v_fma_mix_f32 v245, v15, v15, v245 op_sel_hi:[1,1,0]
	v_fma_mix_f32 v244, v15, 1.0, v244 op_sel:[1,0,0] op_sel_hi:[1,0,0]
	v_fma_mix_f32 v245, v15, v15, v245 op_sel:[1,1,0] op_sel_hi:[1,1,0]
	s_waitcnt vmcnt(12)
	v_fma_mix_f32 v72, v88, v205, v225 op_sel_hi:[1,0,0]
	v_fma_mix_f32 v73, v88, v205, v225 op_sel:[1,0,0] op_sel_hi:[1,0,0]
	v_fma_mix_f32 v74, v89, v205, v225 op_sel_hi:[1,0,0]
	v_fma_mix_f32 v75, v89, v205, v225 op_sel:[1,0,0] op_sel_hi:[1,0,0]
	v_fma_mix_f32 v80, v90, v205, v225 op_sel_hi:[1,0,0]
	v_fma_mix_f32 v81, v90, v205, v225 op_sel:[1,0,0] op_sel_hi:[1,0,0]
	v_fma_mix_f32 v82, v91, v205, v225 op_sel_hi:[1,0,0]
	v_fma_mix_f32 v83, v91, v205, v225 op_sel:[1,0,0] op_sel_hi:[1,0,0]
	v_pk_fma_f32 v[4:5], v[72:73], v[168:169], v[4:5]
	v_pk_fma_f32 v[6:7], v[74:75], v[170:171], v[6:7]
	v_pk_fma_f32 v[0:1], v[80:81], v[172:173], v[0:1]
	v_pk_fma_f32 v[2:3], v[82:83], v[174:175], v[2:3]
	v_cvt_pk_f16_f32 v4, v4, v5
	v_cvt_pk_f16_f32 v5, v6, v7
	v_cvt_pk_f16_f32 v6, v0, v1
	v_cvt_pk_f16_f32 v7, v2, v3
	ds_write_b128 v235, v[4:7] offset:64
	v_fma_mix_f32 v244, v4, 1.0, v244 op_sel_hi:[1,0,0]
	v_fma_mix_f32 v245, v4, v4, v245 op_sel_hi:[1,1,0]
	v_fma_mix_f32 v244, v4, 1.0, v244 op_sel:[1,0,0] op_sel_hi:[1,0,0]
	v_fma_mix_f32 v245, v4, v4, v245 op_sel:[1,1,0] op_sel_hi:[1,1,0]
	v_fma_mix_f32 v244, v5, 1.0, v244 op_sel_hi:[1,0,0]
	v_fma_mix_f32 v245, v5, v5, v245 op_sel_hi:[1,1,0]
	v_fma_mix_f32 v244, v5, 1.0, v244 op_sel:[1,0,0] op_sel_hi:[1,0,0]
	v_fma_mix_f32 v245, v5, v5, v245 op_sel:[1,1,0] op_sel_hi:[1,1,0]
	v_fma_mix_f32 v244, v6, 1.0, v244 op_sel_hi:[1,0,0]
	v_fma_mix_f32 v245, v6, v6, v245 op_sel_hi:[1,1,0]
	v_fma_mix_f32 v244, v6, 1.0, v244 op_sel:[1,0,0] op_sel_hi:[1,0,0]
	v_fma_mix_f32 v245, v6, v6, v245 op_sel:[1,1,0] op_sel_hi:[1,1,0]
	v_fma_mix_f32 v244, v7, 1.0, v244 op_sel_hi:[1,0,0]
	v_fma_mix_f32 v245, v7, v7, v245 op_sel_hi:[1,1,0]
	v_fma_mix_f32 v244, v7, 1.0, v244 op_sel:[1,0,0] op_sel_hi:[1,0,0]
	v_fma_mix_f32 v245, v7, v7, v245 op_sel:[1,1,0] op_sel_hi:[1,1,0]
	ds_read_b128 v[108:111], v236
	ds_read_b128 v[100:103], v236 offset:1152
	s_waitcnt lgkmcnt(0)
	v_add_u32_e32 v83, 0x42000, v224
	buffer_store_dwordx4 v[108:111], v83, s[24:27], 0 offen nt
	v_add_u32_e32 v82, 0x45000, v224
	buffer_store_dwordx4 v[100:103], v82, s[24:27], 0 offen nt
	v_xor_b32_e32 v246, 16, v234
	v_lshlrev_b32_e32 v246, 2, v246
	v_xor_b32_e32 v247, 32, v234
	v_lshlrev_b32_e32 v247, 2, v247
	ds_bpermute_b32 v92, v246, v206
	ds_bpermute_b32 v93, v246, v207
	ds_bpermute_b32 v94, v246, v140
	ds_bpermute_b32 v95, v246, v141
	ds_bpermute_b32 v120, v246, v142
	ds_bpermute_b32 v121, v246, v143
	ds_bpermute_b32 v122, v246, v216
	ds_bpermute_b32 v123, v246, v217
	s_waitcnt lgkmcnt(0)
	v_pk_add_f32 v[206:207], v[206:207], v[92:93]
	v_pk_add_f32 v[140:141], v[140:141], v[94:95]
	v_pk_add_f32 v[142:143], v[142:143], v[120:121]
	v_pk_add_f32 v[216:217], v[216:217], v[122:123]
	ds_bpermute_b32 v92, v246, v218
	ds_bpermute_b32 v93, v246, v219
	ds_bpermute_b32 v94, v246, v208
	ds_bpermute_b32 v95, v246, v209
	ds_bpermute_b32 v120, v246, v210
	ds_bpermute_b32 v121, v246, v211
	ds_bpermute_b32 v122, v246, v244
	ds_bpermute_b32 v123, v246, v245
	s_waitcnt lgkmcnt(0)
	v_pk_add_f32 v[218:219], v[218:219], v[92:93]
	v_pk_add_f32 v[208:209], v[208:209], v[94:95]
	v_pk_add_f32 v[210:211], v[210:211], v[120:121]
	v_pk_add_f32 v[244:245], v[244:245], v[122:123]
	ds_bpermute_b32 v92, v247, v206
	ds_bpermute_b32 v93, v247, v207
	ds_bpermute_b32 v94, v247, v140
	ds_bpermute_b32 v95, v247, v141
	ds_bpermute_b32 v120, v247, v142
	ds_bpermute_b32 v121, v247, v143
	ds_bpermute_b32 v122, v247, v216
	ds_bpermute_b32 v123, v247, v217
	s_waitcnt lgkmcnt(0)
	v_pk_add_f32 v[206:207], v[206:207], v[92:93]
	v_pk_add_f32 v[140:141], v[140:141], v[94:95]
	v_pk_add_f32 v[142:143], v[142:143], v[120:121]
	v_pk_add_f32 v[216:217], v[216:217], v[122:123]
	ds_bpermute_b32 v92, v247, v218
	ds_bpermute_b32 v93, v247, v219
	ds_bpermute_b32 v94, v247, v208
	ds_bpermute_b32 v95, v247, v209
	ds_bpermute_b32 v120, v247, v210
	ds_bpermute_b32 v121, v247, v211
	ds_bpermute_b32 v122, v247, v244
	ds_bpermute_b32 v123, v247, v245
	s_waitcnt lgkmcnt(0)
	v_pk_add_f32 v[218:219], v[218:219], v[92:93]
	v_pk_add_f32 v[208:209], v[208:209], v[94:95]
	v_pk_add_f32 v[210:211], v[210:211], v[120:121]
	v_pk_add_f32 v[244:245], v[244:245], v[122:123]
	s_mov_b64 exec, 0xffff
	global_store_dwordx2 v190, v[206:207], s[100:101] offset:0
	global_store_dwordx2 v190, v[140:141], s[100:101] offset:128
	global_store_dwordx2 v190, v[142:143], s[100:101] offset:256
	global_store_dwordx2 v190, v[216:217], s[100:101] offset:384
	global_store_dwordx2 v190, v[218:219], s[100:101] offset:1024
	global_store_dwordx2 v190, v[208:209], s[100:101] offset:1152
	global_store_dwordx2 v190, v[210:211], s[100:101] offset:1280
	global_store_dwordx2 v190, v[244:245], s[100:101] offset:1408
	s_mov_b64 exec, -1
	s_mov_b32 s83, s81
	s_mov_b32 s84, s82
	s_mov_b64 s[40:41], s[0:1]
	s_mov_b64 s[38:39], s[8:9]
	s_mov_b64 vcc, s[6:7]
	s_cbranch_vccz .LBB8_12
	s_waitcnt vmcnt(0)
	s_cmpk_gt_u32 s44, 0xff
	s_cbranch_scc1 .LBB8_31
	s_barrier

.LBB8_32:
	s_endpgm
	s_endpgm
	s_endpgm
	s_endpgm
	s_endpgm
	s_endpgm
	s_endpgm
	s_endpgm
	.section	.rodata,"a",@progbits
	.p2align	6, 0x0

.LBB10_27:
	s_add_u32 s40, s38, 0xfff40080
	s_addc_u32 s41, s39, -1
	s_cmp_eq_u32 s87, 44
	s_cselect_b32 s43, s9, s41
	s_cselect_b32 s42, s8, s40
	s_cselect_b32 s41, s1, s86
	s_cselect_b32 s40, s0, s85
	s_add_i32 m0, s51, 0xc000
	ds_read_b128 v[136:139], v232
	ds_read_b128 v[148:151], v232 offset:1024
	ds_read_b128 v[152:155], v232 offset:2048
	ds_read_b128 v[156:159], v232 offset:3072
	ds_read_b128 v[160:163], v232 offset:4096
	ds_read_b128 v[164:167], v232 offset:5120
	ds_read_b128 v[168:171], v232 offset:6144
	ds_read_b128 v[172:175], v232 offset:7168
	global_load_lds_dwordx4 v184, s[38:39]
	s_add_i32 m0, s51, 0xe000
	s_nop 0
	global_load_lds_dwordx4 v186, s[38:39]
	s_waitcnt lgkmcnt(8)
	s_barrier
	s_waitcnt lgkmcnt(0)
	v_mfma_f32_16x16x32_f16 v[144:147], v[72:75], v[136:139], v[144:147]
	v_mfma_f32_16x16x32_f16 v[140:143], v[88:91], v[136:139], v[140:143]
	v_mfma_f32_16x16x32_f16 v[124:127], v[72:75], v[152:155], v[124:127]
	v_mfma_f32_16x16x32_f16 v[120:123], v[88:91], v[152:155], v[120:123]
	v_mfma_f32_16x16x32_f16 v[108:111], v[72:75], v[160:163], v[108:111]
	v_mfma_f32_16x16x32_f16 v[104:107], v[88:91], v[160:163], v[104:107]
	v_mfma_f32_16x16x32_f16 v[84:87], v[72:75], v[168:171], v[84:87]
	v_mfma_f32_16x16x32_f16 v[76:79], v[88:91], v[168:171], v[76:79]
	v_mfma_f32_16x16x32_f16 v[144:147], v[80:83], v[148:151], v[144:147]
	v_mfma_f32_16x16x32_f16 v[140:143], v[92:95], v[148:151], v[140:143]
	v_mfma_f32_16x16x32_f16 v[124:127], v[80:83], v[156:159], v[124:127]
	v_mfma_f32_16x16x32_f16 v[120:123], v[92:95], v[156:159], v[120:123]
	v_mfma_f32_16x16x32_f16 v[108:111], v[80:83], v[164:167], v[108:111]
	v_mfma_f32_16x16x32_f16 v[104:107], v[92:95], v[164:167], v[104:107]
	v_mfma_f32_16x16x32_f16 v[84:87], v[80:83], v[172:175], v[84:87]
	v_mfma_f32_16x16x32_f16 v[76:79], v[92:95], v[172:175], v[76:79]
	s_barrier
	s_add_i32 s88, s69, s50
	s_add_u32 s92, s40, 0x80
	s_addc_u32 s93, s41, 0
	s_mov_b32 m0, s88
	ds_read_b128 v[190:193], v233
	ds_read_b128 v[194:197], v233 offset:1024
	ds_read_b128 v[198:201], v233 offset:2048
	ds_read_b128 v[202:205], v233 offset:3072
	global_load_lds_dwordx4 v178, s[40:41]
	s_add_i32 m0, s88, 0x2000
	s_nop 0
	global_load_lds_dwordx4 v182, s[40:41]
	s_barrier
	s_waitcnt lgkmcnt(0)
	v_mfma_f32_16x16x32_f16 v[132:135], v[190:193], v[136:139], v[132:135]
	v_mfma_f32_16x16x32_f16 v[128:131], v[198:201], v[136:139], v[128:131]
	v_mfma_f32_16x16x32_f16 v[116:119], v[190:193], v[152:155], v[116:119]
	v_mfma_f32_16x16x32_f16 v[112:115], v[198:201], v[152:155], v[112:115]
	v_mfma_f32_16x16x32_f16 v[100:103], v[190:193], v[160:163], v[100:103]
	v_mfma_f32_16x16x32_f16 v[96:99], v[198:201], v[160:163], v[96:99]
	v_mfma_f32_16x16x32_f16 v[68:71], v[190:193], v[168:171], v[68:71]
	v_mfma_f32_16x16x32_f16 v[64:67], v[198:201], v[168:171], v[64:67]
	v_mfma_f32_16x16x32_f16 v[132:135], v[194:197], v[148:151], v[132:135]
	v_mfma_f32_16x16x32_f16 v[128:131], v[202:205], v[148:151], v[128:131]
	v_mfma_f32_16x16x32_f16 v[116:119], v[194:197], v[156:159], v[116:119]
	v_mfma_f32_16x16x32_f16 v[112:115], v[202:205], v[156:159], v[112:115]
	v_mfma_f32_16x16x32_f16 v[100:103], v[194:197], v[164:167], v[100:103]
	v_mfma_f32_16x16x32_f16 v[96:99], v[202:205], v[164:167], v[96:99]
	v_mfma_f32_16x16x32_f16 v[68:71], v[194:197], v[172:175], v[68:71]
	v_mfma_f32_16x16x32_f16 v[64:67], v[202:205], v[172:175], v[64:67]
	s_barrier
	s_mov_b32 m0, s51
	s_add_u32 s94, s42, 0x80
	s_addc_u32 s95, s43, 0
	ds_read_b128 v[136:139], v232 offset:16384
	ds_read_b128 v[148:151], v232 offset:17408
	ds_read_b128 v[152:155], v232 offset:18432
	ds_read_b128 v[156:159], v232 offset:19456
	ds_read_b128 v[160:163], v232 offset:20480
	ds_read_b128 v[164:167], v232 offset:21504
	ds_read_b128 v[168:171], v232 offset:22528
	ds_read_b128 v[172:175], v232 offset:23552
	global_load_lds_dwordx4 v176, s[42:43]
	s_mov_b32 m0, s52
	s_nop 0
	global_load_lds_dwordx4 v180, s[42:43]
	s_waitcnt vmcnt(10)
	s_barrier
	s_waitcnt lgkmcnt(0)
	v_mfma_f32_16x16x32_f16 v[60:63], v[72:75], v[136:139], v[60:63]
	v_mfma_f32_16x16x32_f16 v[56:59], v[88:91], v[136:139], v[56:59]
	v_mfma_f32_16x16x32_f16 v[44:47], v[72:75], v[152:155], v[44:47]
	v_mfma_f32_16x16x32_f16 v[40:43], v[88:91], v[152:155], v[40:43]
	v_mfma_f32_16x16x32_f16 v[28:31], v[72:75], v[160:163], v[28:31]
	v_mfma_f32_16x16x32_f16 v[24:27], v[88:91], v[160:163], v[24:27]
	v_mfma_f32_16x16x32_f16 v[12:15], v[72:75], v[168:171], v[12:15]
	v_mfma_f32_16x16x32_f16 v[8:11], v[88:91], v[168:171], v[8:11]
	v_mfma_f32_16x16x32_f16 v[60:63], v[80:83], v[148:151], v[60:63]
	v_mfma_f32_16x16x32_f16 v[56:59], v[92:95], v[148:151], v[56:59]
	v_mfma_f32_16x16x32_f16 v[44:47], v[80:83], v[156:159], v[44:47]
	v_mfma_f32_16x16x32_f16 v[40:43], v[92:95], v[156:159], v[40:43]
	v_mfma_f32_16x16x32_f16 v[28:31], v[80:83], v[164:167], v[28:31]
	v_mfma_f32_16x16x32_f16 v[24:27], v[92:95], v[164:167], v[24:27]
	v_mfma_f32_16x16x32_f16 v[12:15], v[80:83], v[172:175], v[12:15]
	v_mfma_f32_16x16x32_f16 v[8:11], v[92:95], v[172:175], v[8:11]
	s_barrier
	s_add_u32 s88, s40, 0x30000
	s_addc_u32 s89, s41, 0
	s_add_i32 s90, s70, s50
	s_mov_b32 m0, s90
	s_nop 0
	global_load_lds_dwordx4 v178, s[88:89]
	s_add_i32 m0, s90, 0x2000
	s_nop 0
	global_load_lds_dwordx4 v182, s[88:89]
	s_add_i32 s88, 0, 0x18000
	v_add_u32_e32 v92, s88, v228
	ds_read_b128 v[72:75], v92
	ds_read_b128 v[80:83], v92 offset:1024
	ds_read_b128 v[88:91], v92 offset:2048
	ds_read_b128 v[92:95], v92 offset:3072
	s_waitcnt vmcnt(6)
	s_barrier
	v_mfma_f32_16x16x32_f16 v[52:55], v[190:193], v[136:139], v[52:55]
	v_mfma_f32_16x16x32_f16 v[48:51], v[198:201], v[136:139], v[48:51]
	v_mfma_f32_16x16x32_f16 v[36:39], v[190:193], v[152:155], v[36:39]
	v_mfma_f32_16x16x32_f16 v[32:35], v[198:201], v[152:155], v[32:35]
	v_mfma_f32_16x16x32_f16 v[20:23], v[190:193], v[160:163], v[20:23]
	v_mfma_f32_16x16x32_f16 v[16:19], v[198:201], v[160:163], v[16:19]
	v_mfma_f32_16x16x32_f16 v[4:7], v[190:193], v[168:171], v[4:7]
	v_mfma_f32_16x16x32_f16 v[0:3], v[198:201], v[168:171], v[0:3]
	v_mfma_f32_16x16x32_f16 v[52:55], v[194:197], v[148:151], v[52:55]
	v_mfma_f32_16x16x32_f16 v[48:51], v[202:205], v[148:151], v[48:51]
	v_mfma_f32_16x16x32_f16 v[36:39], v[194:197], v[156:159], v[36:39]
	v_mfma_f32_16x16x32_f16 v[32:35], v[202:205], v[156:159], v[32:35]
	v_mfma_f32_16x16x32_f16 v[20:23], v[194:197], v[164:167], v[20:23]
	v_mfma_f32_16x16x32_f16 v[16:19], v[202:205], v[164:167], v[16:19]
	v_mfma_f32_16x16x32_f16 v[4:7], v[194:197], v[172:175], v[4:7]
	v_mfma_f32_16x16x32_f16 v[0:3], v[202:205], v[172:175], v[0:3]
	s_barrier
	s_add_u32 s42, s42, 0xc0000
	s_addc_u32 s43, s43, 0
	s_mov_b32 m0, s53
	ds_read_b128 v[136:139], v232 offset:32768
	ds_read_b128 v[148:151], v232 offset:33792
	ds_read_b128 v[152:155], v232 offset:34816
	ds_read_b128 v[156:159], v232 offset:35840
	ds_read_b128 v[160:163], v232 offset:36864
	ds_read_b128 v[164:167], v232 offset:37888
	ds_read_b128 v[168:171], v232 offset:38912
	ds_read_b128 v[172:175], v232 offset:39936
	global_load_lds_dwordx4 v176, s[42:43]
	s_mov_b32 m0, s54
	s_nop 0
	global_load_lds_dwordx4 v180, s[42:43]
	s_waitcnt lgkmcnt(8)
	s_barrier
	s_waitcnt lgkmcnt(0)
	v_mfma_f32_16x16x32_f16 v[144:147], v[72:75], v[136:139], v[144:147]
	v_mfma_f32_16x16x32_f16 v[140:143], v[88:91], v[136:139], v[140:143]
	v_mfma_f32_16x16x32_f16 v[124:127], v[72:75], v[152:155], v[124:127]
	v_mfma_f32_16x16x32_f16 v[120:123], v[88:91], v[152:155], v[120:123]
	v_mfma_f32_16x16x32_f16 v[108:111], v[72:75], v[160:163], v[108:111]
	v_mfma_f32_16x16x32_f16 v[104:107], v[88:91], v[160:163], v[104:107]
	v_mfma_f32_16x16x32_f16 v[84:87], v[72:75], v[168:171], v[84:87]
	v_mfma_f32_16x16x32_f16 v[76:79], v[88:91], v[168:171], v[76:79]
	v_mfma_f32_16x16x32_f16 v[144:147], v[80:83], v[148:151], v[144:147]
	v_mfma_f32_16x16x32_f16 v[140:143], v[92:95], v[148:151], v[140:143]
	v_mfma_f32_16x16x32_f16 v[124:127], v[80:83], v[156:159], v[124:127]
	v_mfma_f32_16x16x32_f16 v[120:123], v[92:95], v[156:159], v[120:123]
	v_mfma_f32_16x16x32_f16 v[108:111], v[80:83], v[164:167], v[108:111]
	v_mfma_f32_16x16x32_f16 v[104:107], v[92:95], v[164:167], v[104:107]
	v_mfma_f32_16x16x32_f16 v[84:87], v[80:83], v[172:175], v[84:87]
	v_mfma_f32_16x16x32_f16 v[76:79], v[92:95], v[172:175], v[76:79]
	s_barrier
	s_add_i32 s42, 0, 0x1c000
	s_add_i32 s43, s88, s50
	v_add_u32_e32 v202, s42, v228
	s_mov_b32 m0, s43
	ds_read_b128 v[190:193], v202
	ds_read_b128 v[194:197], v202 offset:1024
	ds_read_b128 v[198:201], v202 offset:2048
	ds_read_b128 v[202:205], v202 offset:3072
	global_load_lds_dwordx4 v178, s[92:93]
	s_add_i32 m0, s43, 0x2000
	s_nop 0
	global_load_lds_dwordx4 v182, s[92:93]
	s_barrier
	s_waitcnt lgkmcnt(0)
	v_mfma_f32_16x16x32_f16 v[132:135], v[190:193], v[136:139], v[132:135]
	v_mfma_f32_16x16x32_f16 v[128:131], v[198:201], v[136:139], v[128:131]
	v_mfma_f32_16x16x32_f16 v[116:119], v[190:193], v[152:155], v[116:119]
	v_mfma_f32_16x16x32_f16 v[112:115], v[198:201], v[152:155], v[112:115]
	v_mfma_f32_16x16x32_f16 v[100:103], v[190:193], v[160:163], v[100:103]
	v_mfma_f32_16x16x32_f16 v[96:99], v[198:201], v[160:163], v[96:99]
	v_mfma_f32_16x16x32_f16 v[68:71], v[190:193], v[168:171], v[68:71]
	v_mfma_f32_16x16x32_f16 v[64:67], v[198:201], v[168:171], v[64:67]
	v_mfma_f32_16x16x32_f16 v[132:135], v[194:197], v[148:151], v[132:135]
	v_mfma_f32_16x16x32_f16 v[128:131], v[202:205], v[148:151], v[128:131]
	v_mfma_f32_16x16x32_f16 v[116:119], v[194:197], v[156:159], v[116:119]
	v_mfma_f32_16x16x32_f16 v[112:115], v[202:205], v[156:159], v[112:115]
	v_mfma_f32_16x16x32_f16 v[100:103], v[194:197], v[164:167], v[100:103]
	v_mfma_f32_16x16x32_f16 v[96:99], v[202:205], v[164:167], v[96:99]
	v_mfma_f32_16x16x32_f16 v[68:71], v[194:197], v[172:175], v[68:71]
	v_mfma_f32_16x16x32_f16 v[64:67], v[202:205], v[172:175], v[64:67]
	s_barrier
	s_mov_b32 m0, s58
	ds_read_b128 v[136:139], v232 offset:49152
	ds_read_b128 v[148:151], v232 offset:50176
	ds_read_b128 v[152:155], v232 offset:51200
	ds_read_b128 v[156:159], v232 offset:52224
	ds_read_b128 v[160:163], v232 offset:53248
	ds_read_b128 v[164:167], v232 offset:54272
	ds_read_b128 v[168:171], v232 offset:55296
	ds_read_b128 v[172:175], v232 offset:56320
	global_load_lds_dwordx4 v176, s[94:95]
	s_mov_b32 m0, s59
	s_nop 0
	global_load_lds_dwordx4 v180, s[94:95]
	s_waitcnt vmcnt(10)
	s_barrier
	s_waitcnt lgkmcnt(0)
	v_mfma_f32_16x16x32_f16 v[60:63], v[72:75], v[136:139], v[60:63]
	v_mfma_f32_16x16x32_f16 v[56:59], v[88:91], v[136:139], v[56:59]
	v_mfma_f32_16x16x32_f16 v[44:47], v[72:75], v[152:155], v[44:47]
	v_mfma_f32_16x16x32_f16 v[40:43], v[88:91], v[152:155], v[40:43]
	v_mfma_f32_16x16x32_f16 v[28:31], v[72:75], v[160:163], v[28:31]
	v_mfma_f32_16x16x32_f16 v[24:27], v[88:91], v[160:163], v[24:27]
	v_mfma_f32_16x16x32_f16 v[12:15], v[72:75], v[168:171], v[12:15]
	v_mfma_f32_16x16x32_f16 v[8:11], v[88:91], v[168:171], v[8:11]
	v_mfma_f32_16x16x32_f16 v[60:63], v[80:83], v[148:151], v[60:63]
	v_mfma_f32_16x16x32_f16 v[56:59], v[92:95], v[148:151], v[56:59]
	v_mfma_f32_16x16x32_f16 v[44:47], v[80:83], v[156:159], v[44:47]
	v_mfma_f32_16x16x32_f16 v[40:43], v[92:95], v[156:159], v[40:43]
	v_mfma_f32_16x16x32_f16 v[28:31], v[80:83], v[164:167], v[28:31]
	v_mfma_f32_16x16x32_f16 v[24:27], v[92:95], v[164:167], v[24:27]
	v_mfma_f32_16x16x32_f16 v[12:15], v[80:83], v[172:175], v[12:15]
	v_mfma_f32_16x16x32_f16 v[8:11], v[92:95], v[172:175], v[8:11]
	s_barrier
	s_add_u32 s40, s40, 0x30080
	s_addc_u32 s41, s41, 0
	s_add_i32 s42, s42, s50
	s_mov_b32 m0, s42
	s_nop 0
	global_load_lds_dwordx4 v178, s[40:41]
	s_add_i32 m0, s42, 0x2000
	s_nop 0
	global_load_lds_dwordx4 v182, s[40:41]
	ds_read_b128 v[72:75], v231
	ds_read_b128 v[80:83], v231 offset:1024
	ds_read_b128 v[88:91], v231 offset:2048
	ds_read_b128 v[92:95], v231 offset:3072
	s_waitcnt vmcnt(6)
	s_barrier
	v_mfma_f32_16x16x32_f16 v[52:55], v[190:193], v[136:139], v[52:55]
	v_mfma_f32_16x16x32_f16 v[48:51], v[198:201], v[136:139], v[48:51]
	v_mfma_f32_16x16x32_f16 v[36:39], v[190:193], v[152:155], v[36:39]
	v_mfma_f32_16x16x32_f16 v[32:35], v[198:201], v[152:155], v[32:35]
	v_mfma_f32_16x16x32_f16 v[20:23], v[190:193], v[160:163], v[20:23]
	v_mfma_f32_16x16x32_f16 v[16:19], v[198:201], v[160:163], v[16:19]
	v_mfma_f32_16x16x32_f16 v[4:7], v[190:193], v[168:171], v[4:7]
	v_mfma_f32_16x16x32_f16 v[0:3], v[198:201], v[168:171], v[0:3]
	v_mfma_f32_16x16x32_f16 v[52:55], v[194:197], v[148:151], v[52:55]
	v_mfma_f32_16x16x32_f16 v[48:51], v[202:205], v[148:151], v[48:51]
	v_mfma_f32_16x16x32_f16 v[36:39], v[194:197], v[156:159], v[36:39]
	v_mfma_f32_16x16x32_f16 v[32:35], v[202:205], v[156:159], v[32:35]
	v_mfma_f32_16x16x32_f16 v[20:23], v[194:197], v[164:167], v[20:23]
	v_mfma_f32_16x16x32_f16 v[16:19], v[202:205], v[164:167], v[16:19]
	v_mfma_f32_16x16x32_f16 v[4:7], v[194:197], v[172:175], v[4:7]
	v_mfma_f32_16x16x32_f16 v[0:3], v[202:205], v[172:175], v[0:3]
	s_barrier
	s_add_i32 s87, s87, 2
	s_add_u32 s38, s38, 0x100
	s_addc_u32 s39, s39, 0
	s_add_u32 s85, s85, 0x100
	s_addc_u32 s86, s86, 0
	s_cmp_gt_u32 s87, 45
	s_cbranch_scc0 .LBB10_27
	s_lshl_b32 s92, s84, 8
	s_add_i32 s92, s92, s57
	s_lshl_b32 s93, s83, 8
	s_or_b32 s93, s93, s60
	v_lshlrev_b32_e32 v237, 2, v226
	s_lshl_b32 s96, s93, 2
	s_add_u32 s94, s16, s96
	s_addc_u32 s95, s17, 0
	global_load_dwordx4 v[72:75], v237, s[94:95] offset:0
	global_load_dwordx4 v[80:83], v237, s[94:95] offset:16
	global_load_dwordx4 v[88:91], v237, s[94:95] offset:128
	global_load_dwordx4 v[92:95], v237, s[94:95] offset:144
	s_add_u32 s94, s18, s96
	s_addc_u32 s95, s19, 0
	global_load_dwordx4 v[136:139], v237, s[94:95] offset:0
	global_load_dwordx4 v[148:151], v237, s[94:95] offset:16
	global_load_dwordx4 v[152:155], v237, s[94:95] offset:128
	global_load_dwordx4 v[156:159], v237, s[94:95] offset:144
	s_add_u32 s94, s14, s96
	s_addc_u32 s95, s15, 0
	global_load_dwordx4 v[160:163], v237, s[94:95] offset:0
	global_load_dwordx4 v[164:167], v237, s[94:95] offset:16
	global_load_dwordx4 v[168:171], v237, s[94:95] offset:128
	global_load_dwordx4 v[172:175], v237, s[94:95] offset:144
	v_lshlrev_b32_e32 v190, 3, v227
	s_lshl_b32 s96, s92, 3
	s_add_u32 s94, s12, s96
	s_addc_u32 s95, s13, 0
	global_load_dwordx2 v[238:239], v190, s[94:95] offset:0
	global_load_dwordx2 v[192:193], v190, s[94:95] offset:128
	global_load_dwordx2 v[194:195], v190, s[94:95] offset:256
	global_load_dwordx2 v[196:197], v190, s[94:95] offset:384
	global_load_dwordx2 v[198:199], v190, s[94:95] offset:1024
	global_load_dwordx2 v[200:201], v190, s[94:95] offset:1152
	global_load_dwordx2 v[202:203], v190, s[94:95] offset:1280
	global_load_dwordx2 v[204:205], v190, s[94:95] offset:1408
	v_mul_u32_u24_e32 v191, 0x600, v227
	v_lshl_add_u32 v191, v226, 1, v191
	s_mul_i32 s96, s92, 0x600
	s_lshl_b32 s97, s93, 1
	s_add_u32 s96, s96, s97
	s_add_u32 s98, s10, s96
	s_addc_u32 s99, s11, 0
	s_add_u32 s94, s98, 0x0
	s_addc_u32 s95, s99, 0
	global_load_dwordx4 v[208:211], v191, s[94:95] offset:0 nt
	global_load_dwordx4 v[212:215], v191, s[94:95] offset:64 nt
	s_add_u32 s94, s98, 0x6000
	s_addc_u32 s95, s99, 0
	global_load_dwordx4 v[216:219], v191, s[94:95] offset:0 nt
	global_load_dwordx4 v[220:223], v191, s[94:95] offset:64 nt
	v_add_u32_e32 v224, s92, v229
	v_mul_u32_u24_e32 v224, 0x600, v224
	s_lshl_b32 s97, s93, 1
	v_add3_u32 v224, v224, v230, s97
	s_lshl_b32 s96, s83, 2
	s_lshr_b32 s97, s60, 6
	s_add_u32 s96, s96, s97
	s_lshl_b32 s96, s96, 19
	s_lshl_b32 s97, s92, 3
	s_add_u32 s96, s96, s97
	s_add_u32 s100, s28, s96
	s_addc_u32 s101, s29, 0
	s_waitcnt vmcnt(19)
	v_pk_add_f32 v[72:73], v[72:73], v[136:137]
	v_pk_add_f32 v[74:75], v[74:75], v[138:139]
	s_waitcnt vmcnt(18)
	v_pk_add_f32 v[80:81], v[80:81], v[148:149]
	v_pk_add_f32 v[82:83], v[82:83], v[150:151]
	s_waitcnt vmcnt(17)
	v_pk_add_f32 v[88:89], v[88:89], v[152:153]
	v_pk_add_f32 v[90:91], v[90:91], v[154:155]
	s_waitcnt vmcnt(16)
	v_pk_add_f32 v[92:93], v[92:93], v[156:157]
	v_pk_add_f32 v[94:95], v[94:95], v[158:159]
	v_pk_add_f32 v[144:145], v[144:145], v[72:73]
	v_pk_add_f32 v[146:147], v[146:147], v[74:75]
	v_pk_add_f32 v[124:125], v[124:125], v[72:73]
	v_pk_add_f32 v[126:127], v[126:127], v[74:75]
	v_pk_add_f32 v[108:109], v[108:109], v[72:73]
	v_pk_add_f32 v[110:111], v[110:111], v[74:75]
	v_pk_add_f32 v[84:85], v[84:85], v[72:73]
	v_pk_add_f32 v[86:87], v[86:87], v[74:75]
	v_pk_add_f32 v[60:61], v[60:61], v[72:73]
	v_pk_add_f32 v[62:63], v[62:63], v[74:75]
	v_pk_add_f32 v[44:45], v[44:45], v[72:73]
	v_pk_add_f32 v[46:47], v[46:47], v[74:75]
	v_pk_add_f32 v[28:29], v[28:29], v[72:73]
	v_pk_add_f32 v[30:31], v[30:31], v[74:75]
	v_pk_add_f32 v[12:13], v[12:13], v[72:73]
	v_pk_add_f32 v[14:15], v[14:15], v[74:75]
	v_pk_add_f32 v[140:141], v[140:141], v[80:81]
	v_pk_add_f32 v[142:143], v[142:143], v[82:83]
	v_pk_add_f32 v[120:121], v[120:121], v[80:81]
	v_pk_add_f32 v[122:123], v[122:123], v[82:83]
	v_pk_add_f32 v[104:105], v[104:105], v[80:81]
	v_pk_add_f32 v[106:107], v[106:107], v[82:83]
	v_pk_add_f32 v[76:77], v[76:77], v[80:81]
	v_pk_add_f32 v[78:79], v[78:79], v[82:83]
	v_pk_add_f32 v[56:57], v[56:57], v[80:81]
	v_pk_add_f32 v[58:59], v[58:59], v[82:83]
	v_pk_add_f32 v[40:41], v[40:41], v[80:81]
	v_pk_add_f32 v[42:43], v[42:43], v[82:83]
	v_pk_add_f32 v[24:25], v[24:25], v[80:81]
	v_pk_add_f32 v[26:27], v[26:27], v[82:83]
	v_pk_add_f32 v[8:9], v[8:9], v[80:81]
	v_pk_add_f32 v[10:11], v[10:11], v[82:83]
	v_pk_add_f32 v[132:133], v[132:133], v[88:89]
	v_pk_add_f32 v[134:135], v[134:135], v[90:91]
	v_pk_add_f32 v[116:117], v[116:117], v[88:89]
	v_pk_add_f32 v[118:119], v[118:119], v[90:91]
	v_pk_add_f32 v[100:101], v[100:101], v[88:89]
	v_pk_add_f32 v[102:103], v[102:103], v[90:91]
	v_pk_add_f32 v[68:69], v[68:69], v[88:89]
	v_pk_add_f32 v[70:71], v[70:71], v[90:91]
	v_pk_add_f32 v[52:53], v[52:53], v[88:89]
	v_pk_add_f32 v[54:55], v[54:55], v[90:91]
	v_pk_add_f32 v[36:37], v[36:37], v[88:89]
	v_pk_add_f32 v[38:39], v[38:39], v[90:91]
	v_pk_add_f32 v[20:21], v[20:21], v[88:89]
	v_pk_add_f32 v[22:23], v[22:23], v[90:91]
	v_pk_add_f32 v[4:5], v[4:5], v[88:89]
	v_pk_add_f32 v[6:7], v[6:7], v[90:91]
	v_pk_add_f32 v[128:129], v[128:129], v[92:93]
	v_pk_add_f32 v[130:131], v[130:131], v[94:95]
	v_pk_add_f32 v[112:113], v[112:113], v[92:93]
	v_pk_add_f32 v[114:115], v[114:115], v[94:95]
	v_pk_add_f32 v[96:97], v[96:97], v[92:93]
	v_pk_add_f32 v[98:99], v[98:99], v[94:95]
	v_pk_add_f32 v[64:65], v[64:65], v[92:93]
	v_pk_add_f32 v[66:67], v[66:67], v[94:95]
	v_pk_add_f32 v[48:49], v[48:49], v[92:93]
	v_pk_add_f32 v[50:51], v[50:51], v[94:95]
	v_pk_add_f32 v[32:33], v[32:33], v[92:93]
	v_pk_add_f32 v[34:35], v[34:35], v[94:95]
	v_pk_add_f32 v[16:17], v[16:17], v[92:93]
	v_pk_add_f32 v[18:19], v[18:19], v[94:95]
	v_pk_add_f32 v[0:1], v[0:1], v[92:93]
	v_pk_add_f32 v[2:3], v[2:3], v[94:95]
	s_add_u32 s94, s98, 0xc000
	s_addc_u32 s95, s99, 0
	global_load_dwordx4 v[240:243], v191, s[94:95] offset:0 nt
	global_load_dwordx4 v[244:247], v191, s[94:95] offset:64 nt
	s_add_u32 s94, s98, 0x12000
	s_addc_u32 s95, s99, 0
	global_load_dwordx4 v[248:251], v191, s[94:95] offset:0 nt
	global_load_dwordx4 v[252:255], v191, s[94:95] offset:64 nt
	s_add_u32 s94, s98, 0x30000
	s_addc_u32 s95, s99, 0
	global_load_dwordx4 v[136:139], v191, s[94:95] offset:0 nt
	global_load_dwordx4 v[148:151], v191, s[94:95] offset:64 nt
	s_add_u32 s94, s98, 0x36000
	s_addc_u32 s95, s99, 0
	global_load_dwordx4 v[152:155], v191, s[94:95] offset:0 nt
	global_load_dwordx4 v[156:159], v191, s[94:95] offset:64 nt
	s_waitcnt vmcnt(19)
	v_mul_f32_e64 v225, -v238, v239
	s_waitcnt vmcnt(11)
	v_fma_mix_f32 v72, v208, v239, v225 op_sel_hi:[1,0,0]
	v_fma_mix_f32 v73, v208, v239, v225 op_sel:[1,0,0] op_sel_hi:[1,0,0]
	v_fma_mix_f32 v74, v209, v239, v225 op_sel_hi:[1,0,0]
	v_fma_mix_f32 v75, v209, v239, v225 op_sel:[1,0,0] op_sel_hi:[1,0,0]
	v_fma_mix_f32 v80, v210, v239, v225 op_sel_hi:[1,0,0]
	v_fma_mix_f32 v81, v210, v239, v225 op_sel:[1,0,0] op_sel_hi:[1,0,0]
	v_fma_mix_f32 v82, v211, v239, v225 op_sel_hi:[1,0,0]
	v_fma_mix_f32 v83, v211, v239, v225 op_sel:[1,0,0] op_sel_hi:[1,0,0]
	v_pk_fma_f32 v[144:145], v[72:73], v[160:161], v[144:145]
	v_pk_fma_f32 v[146:147], v[74:75], v[162:163], v[146:147]
	v_pk_fma_f32 v[140:141], v[80:81], v[164:165], v[140:141]
	v_pk_fma_f32 v[142:143], v[82:83], v[166:167], v[142:143]
	v_cvt_pk_f16_f32 v144, v144, v145
	v_cvt_pk_f16_f32 v145, v146, v147
	v_cvt_pk_f16_f32 v146, v140, v141
	v_cvt_pk_f16_f32 v147, v142, v143
	ds_write_b128 v235, v[144:147]
	v_fma_mix_f32 v206, v144, 1.0, 0 op_sel_hi:[1,0,0]
	v_fma_mix_f32 v207, v144, v144, 0 op_sel_hi:[1,1,0]
	v_fma_mix_f32 v206, v144, 1.0, v206 op_sel:[1,0,0] op_sel_hi:[1,0,0]
	v_fma_mix_f32 v207, v144, v144, v207 op_sel:[1,1,0] op_sel_hi:[1,1,0]
	v_fma_mix_f32 v206, v145, 1.0, v206 op_sel_hi:[1,0,0]
	v_fma_mix_f32 v207, v145, v145, v207 op_sel_hi:[1,1,0]
	v_fma_mix_f32 v206, v145, 1.0, v206 op_sel:[1,0,0] op_sel_hi:[1,0,0]
	v_fma_mix_f32 v207, v145, v145, v207 op_sel:[1,1,0] op_sel_hi:[1,1,0]
	v_fma_mix_f32 v206, v146, 1.0, v206 op_sel_hi:[1,0,0]
	v_fma_mix_f32 v207, v146, v146, v207 op_sel_hi:[1,1,0]
	v_fma_mix_f32 v206, v146, 1.0, v206 op_sel:[1,0,0] op_sel_hi:[1,0,0]
	v_fma_mix_f32 v207, v146, v146, v207 op_sel:[1,1,0] op_sel_hi:[1,1,0]
	v_fma_mix_f32 v206, v147, 1.0, v206 op_sel_hi:[1,0,0]
	v_fma_mix_f32 v207, v147, v147, v207 op_sel_hi:[1,1,0]
	v_fma_mix_f32 v206, v147, 1.0, v206 op_sel:[1,0,0] op_sel_hi:[1,0,0]
	v_fma_mix_f32 v207, v147, v147, v207 op_sel:[1,1,0] op_sel_hi:[1,1,0]
	s_waitcnt vmcnt(10)
	v_fma_mix_f32 v72, v212, v239, v225 op_sel_hi:[1,0,0]
	v_fma_mix_f32 v73, v212, v239, v225 op_sel:[1,0,0] op_sel_hi:[1,0,0]
	v_fma_mix_f32 v74, v213, v239, v225 op_sel_hi:[1,0,0]
	v_fma_mix_f32 v75, v213, v239, v225 op_sel:[1,0,0] op_sel_hi:[1,0,0]
	v_fma_mix_f32 v80, v214, v239, v225 op_sel_hi:[1,0,0]
	v_fma_mix_f32 v81, v214, v239, v225 op_sel:[1,0,0] op_sel_hi:[1,0,0]
	v_fma_mix_f32 v82, v215, v239, v225 op_sel_hi:[1,0,0]
	v_fma_mix_f32 v83, v215, v239, v225 op_sel:[1,0,0] op_sel_hi:[1,0,0]
	v_pk_fma_f32 v[132:133], v[72:73], v[168:169], v[132:133]
	v_pk_fma_f32 v[134:135], v[74:75], v[170:171], v[134:135]
	v_pk_fma_f32 v[128:129], v[80:81], v[172:173], v[128:129]
	v_pk_fma_f32 v[130:131], v[82:83], v[174:175], v[130:131]
	v_cvt_pk_f16_f32 v132, v132, v133
	v_cvt_pk_f16_f32 v133, v134, v135
	v_cvt_pk_f16_f32 v134, v128, v129
	v_cvt_pk_f16_f32 v135, v130, v131
	ds_write_b128 v235, v[132:135] offset:64
	v_fma_mix_f32 v206, v132, 1.0, v206 op_sel_hi:[1,0,0]
	v_fma_mix_f32 v207, v132, v132, v207 op_sel_hi:[1,1,0]
	v_fma_mix_f32 v206, v132, 1.0, v206 op_sel:[1,0,0] op_sel_hi:[1,0,0]
	v_fma_mix_f32 v207, v132, v132, v207 op_sel:[1,1,0] op_sel_hi:[1,1,0]
	v_fma_mix_f32 v206, v133, 1.0, v206 op_sel_hi:[1,0,0]
	v_fma_mix_f32 v207, v133, v133, v207 op_sel_hi:[1,1,0]
	v_fma_mix_f32 v206, v133, 1.0, v206 op_sel:[1,0,0] op_sel_hi:[1,0,0]
	v_fma_mix_f32 v207, v133, v133, v207 op_sel:[1,1,0] op_sel_hi:[1,1,0]
	v_fma_mix_f32 v206, v134, 1.0, v206 op_sel_hi:[1,0,0]
	v_fma_mix_f32 v207, v134, v134, v207 op_sel_hi:[1,1,0]
	v_fma_mix_f32 v206, v134, 1.0, v206 op_sel:[1,0,0] op_sel_hi:[1,0,0]
	v_fma_mix_f32 v207, v134, v134, v207 op_sel:[1,1,0] op_sel_hi:[1,1,0]
	v_fma_mix_f32 v206, v135, 1.0, v206 op_sel_hi:[1,0,0]
	v_fma_mix_f32 v207, v135, v135, v207 op_sel_hi:[1,1,0]
	v_fma_mix_f32 v206, v135, 1.0, v206 op_sel:[1,0,0] op_sel_hi:[1,0,0]
	v_fma_mix_f32 v207, v135, v135, v207 op_sel:[1,1,0] op_sel_hi:[1,1,0]
	ds_read_b128 v[88:91], v236
	ds_read_b128 v[92:95], v236 offset:1152
	v_mul_f32_e64 v225, -v192, v193
	s_waitcnt vmcnt(9)
	v_fma_mix_f32 v72, v216, v193, v225 op_sel_hi:[1,0,0]
	v_fma_mix_f32 v73, v216, v193, v225 op_sel:[1,0,0] op_sel_hi:[1,0,0]
	v_fma_mix_f32 v74, v217, v193, v225 op_sel_hi:[1,0,0]
	v_fma_mix_f32 v75, v217, v193, v225 op_sel:[1,0,0] op_sel_hi:[1,0,0]
	v_fma_mix_f32 v80, v218, v193, v225 op_sel_hi:[1,0,0]
	v_fma_mix_f32 v81, v218, v193, v225 op_sel:[1,0,0] op_sel_hi:[1,0,0]
	v_fma_mix_f32 v82, v219, v193, v225 op_sel_hi:[1,0,0]
	v_fma_mix_f32 v83, v219, v193, v225 op_sel:[1,0,0] op_sel_hi:[1,0,0]
	v_pk_fma_f32 v[124:125], v[72:73], v[160:161], v[124:125]
	v_pk_fma_f32 v[126:127], v[74:75], v[162:163], v[126:127]
	v_pk_fma_f32 v[120:121], v[80:81], v[164:165], v[120:121]
	v_pk_fma_f32 v[122:123], v[82:83], v[166:167], v[122:123]
	v_cvt_pk_f16_f32 v124, v124, v125
	v_cvt_pk_f16_f32 v125, v126, v127
	v_cvt_pk_f16_f32 v126, v120, v121
	v_cvt_pk_f16_f32 v127, v122, v123
	s_waitcnt lgkmcnt(0)
	buffer_store_dwordx4 v[88:91], v224, s[24:27], 0 offen nt
	v_add_u32_e32 v82, 0x3000, v224
	buffer_store_dwordx4 v[92:95], v82, s[24:27], 0 offen nt
	ds_write_b128 v235, v[124:127]
	v_fma_mix_f32 v140, v124, 1.0, 0 op_sel_hi:[1,0,0]
	v_fma_mix_f32 v141, v124, v124, 0 op_sel_hi:[1,1,0]
	v_fma_mix_f32 v140, v124, 1.0, v140 op_sel:[1,0,0] op_sel_hi:[1,0,0]
	v_fma_mix_f32 v141, v124, v124, v141 op_sel:[1,1,0] op_sel_hi:[1,1,0]
	v_fma_mix_f32 v140, v125, 1.0, v140 op_sel_hi:[1,0,0]
	v_fma_mix_f32 v141, v125, v125, v141 op_sel_hi:[1,1,0]
	v_fma_mix_f32 v140, v125, 1.0, v140 op_sel:[1,0,0] op_sel_hi:[1,0,0]
	v_fma_mix_f32 v141, v125, v125, v141 op_sel:[1,1,0] op_sel_hi:[1,1,0]
	v_fma_mix_f32 v140, v126, 1.0, v140 op_sel_hi:[1,0,0]
	v_fma_mix_f32 v141, v126, v126, v141 op_sel_hi:[1,1,0]
	v_fma_mix_f32 v140, v126, 1.0, v140 op_sel:[1,0,0] op_sel_hi:[1,0,0]
	v_fma_mix_f32 v141, v126, v126, v141 op_sel:[1,1,0] op_sel_hi:[1,1,0]
	v_fma_mix_f32 v140, v127, 1.0, v140 op_sel_hi:[1,0,0]
	v_fma_mix_f32 v141, v127, v127, v141 op_sel_hi:[1,1,0]
	v_fma_mix_f32 v140, v127, 1.0, v140 op_sel:[1,0,0] op_sel_hi:[1,0,0]
	v_fma_mix_f32 v141, v127, v127, v141 op_sel:[1,1,0] op_sel_hi:[1,1,0]
	s_waitcnt vmcnt(10)
	v_fma_mix_f32 v72, v220, v193, v225 op_sel_hi:[1,0,0]
	v_fma_mix_f32 v73, v220, v193, v225 op_sel:[1,0,0] op_sel_hi:[1,0,0]
	v_fma_mix_f32 v74, v221, v193, v225 op_sel_hi:[1,0,0]
	v_fma_mix_f32 v75, v221, v193, v225 op_sel:[1,0,0] op_sel_hi:[1,0,0]
	v_fma_mix_f32 v80, v222, v193, v225 op_sel_hi:[1,0,0]
	v_fma_mix_f32 v81, v222, v193, v225 op_sel:[1,0,0] op_sel_hi:[1,0,0]
	v_fma_mix_f32 v82, v223, v193, v225 op_sel_hi:[1,0,0]
	v_fma_mix_f32 v83, v223, v193, v225 op_sel:[1,0,0] op_sel_hi:[1,0,0]
	v_pk_fma_f32 v[116:117], v[72:73], v[168:169], v[116:117]
	v_pk_fma_f32 v[118:119], v[74:75], v[170:171], v[118:119]
	v_pk_fma_f32 v[112:113], v[80:81], v[172:173], v[112:113]
	v_pk_fma_f32 v[114:115], v[82:83], v[174:175], v[114:115]
	v_cvt_pk_f16_f32 v116, v116, v117
	v_cvt_pk_f16_f32 v117, v118, v119
	v_cvt_pk_f16_f32 v118, v112, v113
	v_cvt_pk_f16_f32 v119, v114, v115
	ds_write_b128 v235, v[116:119] offset:64
	v_fma_mix_f32 v140, v116, 1.0, v140 op_sel_hi:[1,0,0]
	v_fma_mix_f32 v141, v116, v116, v141 op_sel_hi:[1,1,0]
	v_fma_mix_f32 v140, v116, 1.0, v140 op_sel:[1,0,0] op_sel_hi:[1,0,0]
	v_fma_mix_f32 v141, v116, v116, v141 op_sel:[1,1,0] op_sel_hi:[1,1,0]
	v_fma_mix_f32 v140, v117, 1.0, v140 op_sel_hi:[1,0,0]
	v_fma_mix_f32 v141, v117, v117, v141 op_sel_hi:[1,1,0]
	v_fma_mix_f32 v140, v117, 1.0, v140 op_sel:[1,0,0] op_sel_hi:[1,0,0]
	v_fma_mix_f32 v141, v117, v117, v141 op_sel:[1,1,0] op_sel_hi:[1,1,0]
	v_fma_mix_f32 v140, v118, 1.0, v140 op_sel_hi:[1,0,0]
	v_fma_mix_f32 v141, v118, v118, v141 op_sel_hi:[1,1,0]
	v_fma_mix_f32 v140, v118, 1.0, v140 op_sel:[1,0,0] op_sel_hi:[1,0,0]
	v_fma_mix_f32 v141, v118, v118, v141 op_sel:[1,1,0] op_sel_hi:[1,1,0]
	v_fma_mix_f32 v140, v119, 1.0, v140 op_sel_hi:[1,0,0]
	v_fma_mix_f32 v141, v119, v119, v141 op_sel_hi:[1,1,0]
	v_fma_mix_f32 v140, v119, 1.0, v140 op_sel:[1,0,0] op_sel_hi:[1,0,0]
	v_fma_mix_f32 v141, v119, v119, v141 op_sel:[1,1,0] op_sel_hi:[1,1,0]
	ds_read_b128 v[208:211], v236
	ds_read_b128 v[128:131], v236 offset:1152
	s_add_u32 s94, s98, 0x3c000
	s_addc_u32 s95, s99, 0
	global_load_dwordx4 v[212:215], v191, s[94:95] offset:0 nt
	global_load_dwordx4 v[144:147], v191, s[94:95] offset:64 nt
	s_add_u32 s94, s98, 0x42000
	s_addc_u32 s95, s99, 0
	global_load_dwordx4 v[132:135], v191, s[94:95] offset:0 nt
	global_load_dwordx4 v[88:91], v191, s[94:95] offset:64 nt
	v_mul_f32_e64 v225, -v194, v195
	s_waitcnt vmcnt(13)
	v_fma_mix_f32 v72, v240, v195, v225 op_sel_hi:[1,0,0]
	v_fma_mix_f32 v73, v240, v195, v225 op_sel:[1,0,0] op_sel_hi:[1,0,0]
	v_fma_mix_f32 v74, v241, v195, v225 op_sel_hi:[1,0,0]
	v_fma_mix_f32 v75, v241, v195, v225 op_sel:[1,0,0] op_sel_hi:[1,0,0]
	v_fma_mix_f32 v80, v242, v195, v225 op_sel_hi:[1,0,0]
	v_fma_mix_f32 v81, v242, v195, v225 op_sel:[1,0,0] op_sel_hi:[1,0,0]
	v_fma_mix_f32 v82, v243, v195, v225 op_sel_hi:[1,0,0]
	v_fma_mix_f32 v83, v243, v195, v225 op_sel:[1,0,0] op_sel_hi:[1,0,0]
	v_pk_fma_f32 v[108:109], v[72:73], v[160:161], v[108:109]
	v_pk_fma_f32 v[110:111], v[74:75], v[162:163], v[110:111]
	v_pk_fma_f32 v[104:105], v[80:81], v[164:165], v[104:105]
	v_pk_fma_f32 v[106:107], v[82:83], v[166:167], v[106:107]
	v_cvt_pk_f16_f32 v108, v108, v109
	v_cvt_pk_f16_f32 v109, v110, v111
	v_cvt_pk_f16_f32 v110, v104, v105
	v_cvt_pk_f16_f32 v111, v106, v107
	s_waitcnt lgkmcnt(0)
	v_add_u32_e32 v83, 0x6000, v224
	buffer_store_dwordx4 v[208:211], v83, s[24:27], 0 offen nt
	v_add_u32_e32 v82, 0x9000, v224
	buffer_store_dwordx4 v[128:131], v82, s[24:27], 0 offen nt
	ds_write_b128 v235, v[108:111]
	v_fma_mix_f32 v142, v108, 1.0, 0 op_sel_hi:[1,0,0]
	v_fma_mix_f32 v143, v108, v108, 0 op_sel_hi:[1,1,0]
	v_fma_mix_f32 v142, v108, 1.0, v142 op_sel:[1,0,0] op_sel_hi:[1,0,0]
	v_fma_mix_f32 v143, v108, v108, v143 op_sel:[1,1,0] op_sel_hi:[1,1,0]
	v_fma_mix_f32 v142, v109, 1.0, v142 op_sel_hi:[1,0,0]
	v_fma_mix_f32 v143, v109, v109, v143 op_sel_hi:[1,1,0]
	v_fma_mix_f32 v142, v109, 1.0, v142 op_sel:[1,0,0] op_sel_hi:[1,0,0]
	v_fma_mix_f32 v143, v109, v109, v143 op_sel:[1,1,0] op_sel_hi:[1,1,0]
	v_fma_mix_f32 v142, v110, 1.0, v142 op_sel_hi:[1,0,0]
	v_fma_mix_f32 v143, v110, v110, v143 op_sel_hi:[1,1,0]
	v_fma_mix_f32 v142, v110, 1.0, v142 op_sel:[1,0,0] op_sel_hi:[1,0,0]
	v_fma_mix_f32 v143, v110, v110, v143 op_sel:[1,1,0] op_sel_hi:[1,1,0]
	v_fma_mix_f32 v142, v111, 1.0, v142 op_sel_hi:[1,0,0]
	v_fma_mix_f32 v143, v111, v111, v143 op_sel_hi:[1,1,0]
	v_fma_mix_f32 v142, v111, 1.0, v142 op_sel:[1,0,0] op_sel_hi:[1,0,0]
	v_fma_mix_f32 v143, v111, v111, v143 op_sel:[1,1,0] op_sel_hi:[1,1,0]
	s_waitcnt vmcnt(14)
	v_fma_mix_f32 v72, v244, v195, v225 op_sel_hi:[1,0,0]
	v_fma_mix_f32 v73, v244, v195, v225 op_sel:[1,0,0] op_sel_hi:[1,0,0]
	v_fma_mix_f32 v74, v245, v195, v225 op_sel_hi:[1,0,0]
	v_fma_mix_f32 v75, v245, v195, v225 op_sel:[1,0,0] op_sel_hi:[1,0,0]
	v_fma_mix_f32 v80, v246, v195, v225 op_sel_hi:[1,0,0]
	v_fma_mix_f32 v81, v246, v195, v225 op_sel:[1,0,0] op_sel_hi:[1,0,0]
	v_fma_mix_f32 v82, v247, v195, v225 op_sel_hi:[1,0,0]
	v_fma_mix_f32 v83, v247, v195, v225 op_sel:[1,0,0] op_sel_hi:[1,0,0]
	v_pk_fma_f32 v[100:101], v[72:73], v[168:169], v[100:101]
	v_pk_fma_f32 v[102:103], v[74:75], v[170:171], v[102:103]
	v_pk_fma_f32 v[96:97], v[80:81], v[172:173], v[96:97]
	v_pk_fma_f32 v[98:99], v[82:83], v[174:175], v[98:99]
	v_cvt_pk_f16_f32 v100, v100, v101
	v_cvt_pk_f16_f32 v101, v102, v103
	v_cvt_pk_f16_f32 v102, v96, v97
	v_cvt_pk_f16_f32 v103, v98, v99
	ds_write_b128 v235, v[100:103] offset:64
	v_fma_mix_f32 v142, v100, 1.0, v142 op_sel_hi:[1,0,0]
	v_fma_mix_f32 v143, v100, v100, v143 op_sel_hi:[1,1,0]
	v_fma_mix_f32 v142, v100, 1.0, v142 op_sel:[1,0,0] op_sel_hi:[1,0,0]
	v_fma_mix_f32 v143, v100, v100, v143 op_sel:[1,1,0] op_sel_hi:[1,1,0]
	v_fma_mix_f32 v142, v101, 1.0, v142 op_sel_hi:[1,0,0]
	v_fma_mix_f32 v143, v101, v101, v143 op_sel_hi:[1,1,0]
	v_fma_mix_f32 v142, v101, 1.0, v142 op_sel:[1,0,0] op_sel_hi:[1,0,0]
	v_fma_mix_f32 v143, v101, v101, v143 op_sel:[1,1,0] op_sel_hi:[1,1,0]
	v_fma_mix_f32 v142, v102, 1.0, v142 op_sel_hi:[1,0,0]
	v_fma_mix_f32 v143, v102, v102, v143 op_sel_hi:[1,1,0]
	v_fma_mix_f32 v142, v102, 1.0, v142 op_sel:[1,0,0] op_sel_hi:[1,0,0]
	v_fma_mix_f32 v143, v102, v102, v143 op_sel:[1,1,0] op_sel_hi:[1,1,0]
	v_fma_mix_f32 v142, v103, 1.0, v142 op_sel_hi:[1,0,0]
	v_fma_mix_f32 v143, v103, v103, v143 op_sel_hi:[1,1,0]
	v_fma_mix_f32 v142, v103, 1.0, v142 op_sel:[1,0,0] op_sel_hi:[1,0,0]
	v_fma_mix_f32 v143, v103, v103, v143 op_sel:[1,1,0] op_sel_hi:[1,1,0]
	ds_read_b128 v[92:95], v236
	ds_read_b128 v[120:123], v236 offset:1152
	v_mul_f32_e64 v225, -v196, v197
	s_waitcnt vmcnt(13)
	v_fma_mix_f32 v72, v248, v197, v225 op_sel_hi:[1,0,0]
	v_fma_mix_f32 v73, v248, v197, v225 op_sel:[1,0,0] op_sel_hi:[1,0,0]
	v_fma_mix_f32 v74, v249, v197, v225 op_sel_hi:[1,0,0]
	v_fma_mix_f32 v75, v249, v197, v225 op_sel:[1,0,0] op_sel_hi:[1,0,0]
	v_fma_mix_f32 v80, v250, v197, v225 op_sel_hi:[1,0,0]
	v_fma_mix_f32 v81, v250, v197, v225 op_sel:[1,0,0] op_sel_hi:[1,0,0]
	v_fma_mix_f32 v82, v251, v197, v225 op_sel_hi:[1,0,0]
	v_fma_mix_f32 v83, v251, v197, v225 op_sel:[1,0,0] op_sel_hi:[1,0,0]
	v_pk_fma_f32 v[84:85], v[72:73], v[160:161], v[84:85]
	v_pk_fma_f32 v[86:87], v[74:75], v[162:163], v[86:87]
	v_pk_fma_f32 v[76:77], v[80:81], v[164:165], v[76:77]
	v_pk_fma_f32 v[78:79], v[82:83], v[166:167], v[78:79]
	v_cvt_pk_f16_f32 v84, v84, v85
	v_cvt_pk_f16_f32 v85, v86, v87
	v_cvt_pk_f16_f32 v86, v76, v77
	v_cvt_pk_f16_f32 v87, v78, v79
	s_waitcnt lgkmcnt(0)
	v_add_u32_e32 v83, 0xc000, v224
	buffer_store_dwordx4 v[92:95], v83, s[24:27], 0 offen nt
	v_add_u32_e32 v82, 0xf000, v224
	buffer_store_dwordx4 v[120:123], v82, s[24:27], 0 offen nt
	ds_write_b128 v235, v[84:87]
	v_fma_mix_f32 v216, v84, 1.0, 0 op_sel_hi:[1,0,0]
	v_fma_mix_f32 v217, v84, v84, 0 op_sel_hi:[1,1,0]
	v_fma_mix_f32 v216, v84, 1.0, v216 op_sel:[1,0,0] op_sel_hi:[1,0,0]
	v_fma_mix_f32 v217, v84, v84, v217 op_sel:[1,1,0] op_sel_hi:[1,1,0]
	v_fma_mix_f32 v216, v85, 1.0, v216 op_sel_hi:[1,0,0]
	v_fma_mix_f32 v217, v85, v85, v217 op_sel_hi:[1,1,0]
	v_fma_mix_f32 v216, v85, 1.0, v216 op_sel:[1,0,0] op_sel_hi:[1,0,0]
	v_fma_mix_f32 v217, v85, v85, v217 op_sel:[1,1,0] op_sel_hi:[1,1,0]
	v_fma_mix_f32 v216, v86, 1.0, v216 op_sel_hi:[1,0,0]
	v_fma_mix_f32 v217, v86, v86, v217 op_sel_hi:[1,1,0]
	v_fma_mix_f32 v216, v86, 1.0, v216 op_sel:[1,0,0] op_sel_hi:[1,0,0]
	v_fma_mix_f32 v217, v86, v86, v217 op_sel:[1,1,0] op_sel_hi:[1,1,0]
	v_fma_mix_f32 v216, v87, 1.0, v216 op_sel_hi:[1,0,0]
	v_fma_mix_f32 v217, v87, v87, v217 op_sel_hi:[1,1,0]
	v_fma_mix_f32 v216, v87, 1.0, v216 op_sel:[1,0,0] op_sel_hi:[1,0,0]
	v_fma_mix_f32 v217, v87, v87, v217 op_sel:[1,1,0] op_sel_hi:[1,1,0]
	s_waitcnt vmcnt(14)
	v_fma_mix_f32 v72, v252, v197, v225 op_sel_hi:[1,0,0]
	v_fma_mix_f32 v73, v252, v197, v225 op_sel:[1,0,0] op_sel_hi:[1,0,0]
	v_fma_mix_f32 v74, v253, v197, v225 op_sel_hi:[1,0,0]
	v_fma_mix_f32 v75, v253, v197, v225 op_sel:[1,0,0] op_sel_hi:[1,0,0]
	v_fma_mix_f32 v80, v254, v197, v225 op_sel_hi:[1,0,0]
	v_fma_mix_f32 v81, v254, v197, v225 op_sel:[1,0,0] op_sel_hi:[1,0,0]
	v_fma_mix_f32 v82, v255, v197, v225 op_sel_hi:[1,0,0]
	v_fma_mix_f32 v83, v255, v197, v225 op_sel:[1,0,0] op_sel_hi:[1,0,0]
	v_pk_fma_f32 v[68:69], v[72:73], v[168:169], v[68:69]
	v_pk_fma_f32 v[70:71], v[74:75], v[170:171], v[70:71]
	v_pk_fma_f32 v[64:65], v[80:81], v[172:173], v[64:65]
	v_pk_fma_f32 v[66:67], v[82:83], v[174:175], v[66:67]
	v_cvt_pk_f16_f32 v68, v68, v69
	v_cvt_pk_f16_f32 v69, v70, v71
	v_cvt_pk_f16_f32 v70, v64, v65
	v_cvt_pk_f16_f32 v71, v66, v67
	ds_write_b128 v235, v[68:71] offset:64
	v_fma_mix_f32 v216, v68, 1.0, v216 op_sel_hi:[1,0,0]
	v_fma_mix_f32 v217, v68, v68, v217 op_sel_hi:[1,1,0]
	v_fma_mix_f32 v216, v68, 1.0, v216 op_sel:[1,0,0] op_sel_hi:[1,0,0]
	v_fma_mix_f32 v217, v68, v68, v217 op_sel:[1,1,0] op_sel_hi:[1,1,0]
	v_fma_mix_f32 v216, v69, 1.0, v216 op_sel_hi:[1,0,0]
	v_fma_mix_f32 v217, v69, v69, v217 op_sel_hi:[1,1,0]
	v_fma_mix_f32 v216, v69, 1.0, v216 op_sel:[1,0,0] op_sel_hi:[1,0,0]
	v_fma_mix_f32 v217, v69, v69, v217 op_sel:[1,1,0] op_sel_hi:[1,1,0]
	v_fma_mix_f32 v216, v70, 1.0, v216 op_sel_hi:[1,0,0]
	v_fma_mix_f32 v217, v70, v70, v217 op_sel_hi:[1,1,0]
	v_fma_mix_f32 v216, v70, 1.0, v216 op_sel:[1,0,0] op_sel_hi:[1,0,0]
	v_fma_mix_f32 v217, v70, v70, v217 op_sel:[1,1,0] op_sel_hi:[1,1,0]
	v_fma_mix_f32 v216, v71, 1.0, v216 op_sel_hi:[1,0,0]
	v_fma_mix_f32 v217, v71, v71, v217 op_sel_hi:[1,1,0]
	v_fma_mix_f32 v216, v71, 1.0, v216 op_sel:[1,0,0] op_sel_hi:[1,0,0]
	v_fma_mix_f32 v217, v71, v71, v217 op_sel:[1,1,0] op_sel_hi:[1,1,0]
	ds_read_b128 v[112:115], v236
	ds_read_b128 v[220:223], v236 offset:1152
	v_mul_f32_e64 v225, -v198, v199
	s_waitcnt vmcnt(13)
	v_fma_mix_f32 v72, v136, v199, v225 op_sel_hi:[1,0,0]
	v_fma_mix_f32 v73, v136, v199, v225 op_sel:[1,0,0] op_sel_hi:[1,0,0]
	v_fma_mix_f32 v74, v137, v199, v225 op_sel_hi:[1,0,0]
	v_fma_mix_f32 v75, v137, v199, v225 op_sel:[1,0,0] op_sel_hi:[1,0,0]
	v_fma_mix_f32 v80, v138, v199, v225 op_sel_hi:[1,0,0]
	v_fma_mix_f32 v81, v138, v199, v225 op_sel:[1,0,0] op_sel_hi:[1,0,0]
	v_fma_mix_f32 v82, v139, v199, v225 op_sel_hi:[1,0,0]
	v_fma_mix_f32 v83, v139, v199, v225 op_sel:[1,0,0] op_sel_hi:[1,0,0]
	v_pk_fma_f32 v[60:61], v[72:73], v[160:161], v[60:61]
	v_pk_fma_f32 v[62:63], v[74:75], v[162:163], v[62:63]
	v_pk_fma_f32 v[56:57], v[80:81], v[164:165], v[56:57]
	v_pk_fma_f32 v[58:59], v[82:83], v[166:167], v[58:59]
	v_cvt_pk_f16_f32 v60, v60, v61
	v_cvt_pk_f16_f32 v61, v62, v63
	v_cvt_pk_f16_f32 v62, v56, v57
	v_cvt_pk_f16_f32 v63, v58, v59
	s_waitcnt lgkmcnt(0)
	v_add_u32_e32 v83, 0x12000, v224
	buffer_store_dwordx4 v[112:115], v83, s[24:27], 0 offen nt
	v_add_u32_e32 v82, 0x15000, v224
	buffer_store_dwordx4 v[220:223], v82, s[24:27], 0 offen nt
	ds_write_b128 v235, v[60:63]
	v_fma_mix_f32 v218, v60, 1.0, 0 op_sel_hi:[1,0,0]
	v_fma_mix_f32 v219, v60, v60, 0 op_sel_hi:[1,1,0]
	v_fma_mix_f32 v218, v60, 1.0, v218 op_sel:[1,0,0] op_sel_hi:[1,0,0]
	v_fma_mix_f32 v219, v60, v60, v219 op_sel:[1,1,0] op_sel_hi:[1,1,0]
	v_fma_mix_f32 v218, v61, 1.0, v218 op_sel_hi:[1,0,0]
	v_fma_mix_f32 v219, v61, v61, v219 op_sel_hi:[1,1,0]
	v_fma_mix_f32 v218, v61, 1.0, v218 op_sel:[1,0,0] op_sel_hi:[1,0,0]
	v_fma_mix_f32 v219, v61, v61, v219 op_sel:[1,1,0] op_sel_hi:[1,1,0]
	v_fma_mix_f32 v218, v62, 1.0, v218 op_sel_hi:[1,0,0]
	v_fma_mix_f32 v219, v62, v62, v219 op_sel_hi:[1,1,0]
	v_fma_mix_f32 v218, v62, 1.0, v218 op_sel:[1,0,0] op_sel_hi:[1,0,0]
	v_fma_mix_f32 v219, v62, v62, v219 op_sel:[1,1,0] op_sel_hi:[1,1,0]
	v_fma_mix_f32 v218, v63, 1.0, v218 op_sel_hi:[1,0,0]
	v_fma_mix_f32 v219, v63, v63, v219 op_sel_hi:[1,1,0]
	v_fma_mix_f32 v218, v63, 1.0, v218 op_sel:[1,0,0] op_sel_hi:[1,0,0]
	v_fma_mix_f32 v219, v63, v63, v219 op_sel:[1,1,0] op_sel_hi:[1,1,0]
	s_waitcnt vmcnt(14)
	v_fma_mix_f32 v72, v148, v199, v225 op_sel_hi:[1,0,0]
	v_fma_mix_f32 v73, v148, v199, v225 op_sel:[1,0,0] op_sel_hi:[1,0,0]
	v_fma_mix_f32 v74, v149, v199, v225 op_sel_hi:[1,0,0]
	v_fma_mix_f32 v75, v149, v199, v225 op_sel:[1,0,0] op_sel_hi:[1,0,0]
	v_fma_mix_f32 v80, v150, v199, v225 op_sel_hi:[1,0,0]
	v_fma_mix_f32 v81, v150, v199, v225 op_sel:[1,0,0] op_sel_hi:[1,0,0]
	v_fma_mix_f32 v82, v151, v199, v225 op_sel_hi:[1,0,0]
	v_fma_mix_f32 v83, v151, v199, v225 op_sel:[1,0,0] op_sel_hi:[1,0,0]
	v_pk_fma_f32 v[52:53], v[72:73], v[168:169], v[52:53]
	v_pk_fma_f32 v[54:55], v[74:75], v[170:171], v[54:55]
	v_pk_fma_f32 v[48:49], v[80:81], v[172:173], v[48:49]
	v_pk_fma_f32 v[50:51], v[82:83], v[174:175], v[50:51]
	v_cvt_pk_f16_f32 v52, v52, v53
	v_cvt_pk_f16_f32 v53, v54, v55
	v_cvt_pk_f16_f32 v54, v48, v49
	v_cvt_pk_f16_f32 v55, v50, v51
	ds_write_b128 v235, v[52:55] offset:64
	v_fma_mix_f32 v218, v52, 1.0, v218 op_sel_hi:[1,0,0]
	v_fma_mix_f32 v219, v52, v52, v219 op_sel_hi:[1,1,0]
	v_fma_mix_f32 v218, v52, 1.0, v218 op_sel:[1,0,0] op_sel_hi:[1,0,0]
	v_fma_mix_f32 v219, v52, v52, v219 op_sel:[1,1,0] op_sel_hi:[1,1,0]
	v_fma_mix_f32 v218, v53, 1.0, v218 op_sel_hi:[1,0,0]
	v_fma_mix_f32 v219, v53, v53, v219 op_sel_hi:[1,1,0]
	v_fma_mix_f32 v218, v53, 1.0, v218 op_sel:[1,0,0] op_sel_hi:[1,0,0]
	v_fma_mix_f32 v219, v53, v53, v219 op_sel:[1,1,0] op_sel_hi:[1,1,0]
	v_fma_mix_f32 v218, v54, 1.0, v218 op_sel_hi:[1,0,0]
	v_fma_mix_f32 v219, v54, v54, v219 op_sel_hi:[1,1,0]
	v_fma_mix_f32 v218, v54, 1.0, v218 op_sel:[1,0,0] op_sel_hi:[1,0,0]
	v_fma_mix_f32 v219, v54, v54, v219 op_sel:[1,1,0] op_sel_hi:[1,1,0]
	v_fma_mix_f32 v218, v55, 1.0, v218 op_sel_hi:[1,0,0]
	v_fma_mix_f32 v219, v55, v55, v219 op_sel_hi:[1,1,0]
	v_fma_mix_f32 v218, v55, 1.0, v218 op_sel:[1,0,0] op_sel_hi:[1,0,0]
	v_fma_mix_f32 v219, v55, v55, v219 op_sel:[1,1,0] op_sel_hi:[1,1,0]
	ds_read_b128 v[124:127], v236
	ds_read_b128 v[116:119], v236 offset:1152
	v_mul_f32_e64 v225, -v200, v201
	s_waitcnt vmcnt(13)
	v_fma_mix_f32 v72, v152, v201, v225 op_sel_hi:[1,0,0]
	v_fma_mix_f32 v73, v152, v201, v225 op_sel:[1,0,0] op_sel_hi:[1,0,0]
	v_fma_mix_f32 v74, v153, v201, v225 op_sel_hi:[1,0,0]
	v_fma_mix_f32 v75, v153, v201, v225 op_sel:[1,0,0] op_sel_hi:[1,0,0]
	v_fma_mix_f32 v80, v154, v201, v225 op_sel_hi:[1,0,0]
	v_fma_mix_f32 v81, v154, v201, v225 op_sel:[1,0,0] op_sel_hi:[1,0,0]
	v_fma_mix_f32 v82, v155, v201, v225 op_sel_hi:[1,0,0]
	v_fma_mix_f32 v83, v155, v201, v225 op_sel:[1,0,0] op_sel_hi:[1,0,0]
	v_pk_fma_f32 v[44:45], v[72:73], v[160:161], v[44:45]
	v_pk_fma_f32 v[46:47], v[74:75], v[162:163], v[46:47]
	v_pk_fma_f32 v[40:41], v[80:81], v[164:165], v[40:41]
	v_pk_fma_f32 v[42:43], v[82:83], v[166:167], v[42:43]
	v_cvt_pk_f16_f32 v44, v44, v45
	v_cvt_pk_f16_f32 v45, v46, v47
	v_cvt_pk_f16_f32 v46, v40, v41
	v_cvt_pk_f16_f32 v47, v42, v43
	s_waitcnt lgkmcnt(0)
	v_add_u32_e32 v83, 0x30000, v224
	buffer_store_dwordx4 v[124:127], v83, s[24:27], 0 offen nt
	v_add_u32_e32 v82, 0x33000, v224
	buffer_store_dwordx4 v[116:119], v82, s[24:27], 0 offen nt
	ds_write_b128 v235, v[44:47]
	v_fma_mix_f32 v208, v44, 1.0, 0 op_sel_hi:[1,0,0]
	v_fma_mix_f32 v209, v44, v44, 0 op_sel_hi:[1,1,0]
	v_fma_mix_f32 v208, v44, 1.0, v208 op_sel:[1,0,0] op_sel_hi:[1,0,0]
	v_fma_mix_f32 v209, v44, v44, v209 op_sel:[1,1,0] op_sel_hi:[1,1,0]
	v_fma_mix_f32 v208, v45, 1.0, v208 op_sel_hi:[1,0,0]
	v_fma_mix_f32 v209, v45, v45, v209 op_sel_hi:[1,1,0]
	v_fma_mix_f32 v208, v45, 1.0, v208 op_sel:[1,0,0] op_sel_hi:[1,0,0]
	v_fma_mix_f32 v209, v45, v45, v209 op_sel:[1,1,0] op_sel_hi:[1,1,0]
	v_fma_mix_f32 v208, v46, 1.0, v208 op_sel_hi:[1,0,0]
	v_fma_mix_f32 v209, v46, v46, v209 op_sel_hi:[1,1,0]
	v_fma_mix_f32 v208, v46, 1.0, v208 op_sel:[1,0,0] op_sel_hi:[1,0,0]
	v_fma_mix_f32 v209, v46, v46, v209 op_sel:[1,1,0] op_sel_hi:[1,1,0]
	v_fma_mix_f32 v208, v47, 1.0, v208 op_sel_hi:[1,0,0]
	v_fma_mix_f32 v209, v47, v47, v209 op_sel_hi:[1,1,0]
	v_fma_mix_f32 v208, v47, 1.0, v208 op_sel:[1,0,0] op_sel_hi:[1,0,0]
	v_fma_mix_f32 v209, v47, v47, v209 op_sel:[1,1,0] op_sel_hi:[1,1,0]
	s_waitcnt vmcnt(14)
	v_fma_mix_f32 v72, v156, v201, v225 op_sel_hi:[1,0,0]
	v_fma_mix_f32 v73, v156, v201, v225 op_sel:[1,0,0] op_sel_hi:[1,0,0]
	v_fma_mix_f32 v74, v157, v201, v225 op_sel_hi:[1,0,0]
	v_fma_mix_f32 v75, v157, v201, v225 op_sel:[1,0,0] op_sel_hi:[1,0,0]
	v_fma_mix_f32 v80, v158, v201, v225 op_sel_hi:[1,0,0]
	v_fma_mix_f32 v81, v158, v201, v225 op_sel:[1,0,0] op_sel_hi:[1,0,0]
	v_fma_mix_f32 v82, v159, v201, v225 op_sel_hi:[1,0,0]
	v_fma_mix_f32 v83, v159, v201, v225 op_sel:[1,0,0] op_sel_hi:[1,0,0]
	v_pk_fma_f32 v[36:37], v[72:73], v[168:169], v[36:37]
	v_pk_fma_f32 v[38:39], v[74:75], v[170:171], v[38:39]
	v_pk_fma_f32 v[32:33], v[80:81], v[172:173], v[32:33]
	v_pk_fma_f32 v[34:35], v[82:83], v[174:175], v[34:35]
	v_cvt_pk_f16_f32 v36, v36, v37
	v_cvt_pk_f16_f32 v37, v38, v39
	v_cvt_pk_f16_f32 v38, v32, v33
	v_cvt_pk_f16_f32 v39, v34, v35
	ds_write_b128 v235, v[36:39] offset:64
	v_fma_mix_f32 v208, v36, 1.0, v208 op_sel_hi:[1,0,0]
	v_fma_mix_f32 v209, v36, v36, v209 op_sel_hi:[1,1,0]
	v_fma_mix_f32 v208, v36, 1.0, v208 op_sel:[1,0,0] op_sel_hi:[1,0,0]
	v_fma_mix_f32 v209, v36, v36, v209 op_sel:[1,1,0] op_sel_hi:[1,1,0]
	v_fma_mix_f32 v208, v37, 1.0, v208 op_sel_hi:[1,0,0]
	v_fma_mix_f32 v209, v37, v37, v209 op_sel_hi:[1,1,0]
	v_fma_mix_f32 v208, v37, 1.0, v208 op_sel:[1,0,0] op_sel_hi:[1,0,0]
	v_fma_mix_f32 v209, v37, v37, v209 op_sel:[1,1,0] op_sel_hi:[1,1,0]
	v_fma_mix_f32 v208, v38, 1.0, v208 op_sel_hi:[1,0,0]
	v_fma_mix_f32 v209, v38, v38, v209 op_sel_hi:[1,1,0]
	v_fma_mix_f32 v208, v38, 1.0, v208 op_sel:[1,0,0] op_sel_hi:[1,0,0]
	v_fma_mix_f32 v209, v38, v38, v209 op_sel:[1,1,0] op_sel_hi:[1,1,0]
	v_fma_mix_f32 v208, v39, 1.0, v208 op_sel_hi:[1,0,0]
	v_fma_mix_f32 v209, v39, v39, v209 op_sel_hi:[1,1,0]
	v_fma_mix_f32 v208, v39, 1.0, v208 op_sel:[1,0,0] op_sel_hi:[1,0,0]
	v_fma_mix_f32 v209, v39, v39, v209 op_sel:[1,1,0] op_sel_hi:[1,1,0]
	ds_read_b128 v[128:131], v236
	ds_read_b128 v[104:107], v236 offset:1152
	v_mul_f32_e64 v225, -v202, v203
	s_waitcnt vmcnt(11)
	v_fma_mix_f32 v72, v212, v203, v225 op_sel_hi:[1,0,0]
	v_fma_mix_f32 v73, v212, v203, v225 op_sel:[1,0,0] op_sel_hi:[1,0,0]
	v_fma_mix_f32 v74, v213, v203, v225 op_sel_hi:[1,0,0]
	v_fma_mix_f32 v75, v213, v203, v225 op_sel:[1,0,0] op_sel_hi:[1,0,0]
	v_fma_mix_f32 v80, v214, v203, v225 op_sel_hi:[1,0,0]
	v_fma_mix_f32 v81, v214, v203, v225 op_sel:[1,0,0] op_sel_hi:[1,0,0]
	v_fma_mix_f32 v82, v215, v203, v225 op_sel_hi:[1,0,0]
	v_fma_mix_f32 v83, v215, v203, v225 op_sel:[1,0,0] op_sel_hi:[1,0,0]
	v_pk_fma_f32 v[28:29], v[72:73], v[160:161], v[28:29]
	v_pk_fma_f32 v[30:31], v[74:75], v[162:163], v[30:31]
	v_pk_fma_f32 v[24:25], v[80:81], v[164:165], v[24:25]
	v_pk_fma_f32 v[26:27], v[82:83], v[166:167], v[26:27]
	v_cvt_pk_f16_f32 v28, v28, v29
	v_cvt_pk_f16_f32 v29, v30, v31
	v_cvt_pk_f16_f32 v30, v24, v25
	v_cvt_pk_f16_f32 v31, v26, v27
	s_waitcnt lgkmcnt(0)
	v_add_u32_e32 v83, 0x36000, v224
	buffer_store_dwordx4 v[128:131], v83, s[24:27], 0 offen nt
	v_add_u32_e32 v82, 0x39000, v224
	buffer_store_dwordx4 v[104:107], v82, s[24:27], 0 offen nt
	ds_write_b128 v235, v[28:31]
	v_fma_mix_f32 v210, v28, 1.0, 0 op_sel_hi:[1,0,0]
	v_fma_mix_f32 v211, v28, v28, 0 op_sel_hi:[1,1,0]
	v_fma_mix_f32 v210, v28, 1.0, v210 op_sel:[1,0,0] op_sel_hi:[1,0,0]
	v_fma_mix_f32 v211, v28, v28, v211 op_sel:[1,1,0] op_sel_hi:[1,1,0]
	v_fma_mix_f32 v210, v29, 1.0, v210 op_sel_hi:[1,0,0]
	v_fma_mix_f32 v211, v29, v29, v211 op_sel_hi:[1,1,0]
	v_fma_mix_f32 v210, v29, 1.0, v210 op_sel:[1,0,0] op_sel_hi:[1,0,0]
	v_fma_mix_f32 v211, v29, v29, v211 op_sel:[1,1,0] op_sel_hi:[1,1,0]
	v_fma_mix_f32 v210, v30, 1.0, v210 op_sel_hi:[1,0,0]
	v_fma_mix_f32 v211, v30, v30, v211 op_sel_hi:[1,1,0]
	v_fma_mix_f32 v210, v30, 1.0, v210 op_sel:[1,0,0] op_sel_hi:[1,0,0]
	v_fma_mix_f32 v211, v30, v30, v211 op_sel:[1,1,0] op_sel_hi:[1,1,0]
	v_fma_mix_f32 v210, v31, 1.0, v210 op_sel_hi:[1,0,0]
	v_fma_mix_f32 v211, v31, v31, v211 op_sel_hi:[1,1,0]
	v_fma_mix_f32 v210, v31, 1.0, v210 op_sel:[1,0,0] op_sel_hi:[1,0,0]
	v_fma_mix_f32 v211, v31, v31, v211 op_sel:[1,1,0] op_sel_hi:[1,1,0]
	s_waitcnt vmcnt(12)
	v_fma_mix_f32 v72, v144, v203, v225 op_sel_hi:[1,0,0]
	v_fma_mix_f32 v73, v144, v203, v225 op_sel:[1,0,0] op_sel_hi:[1,0,0]
	v_fma_mix_f32 v74, v145, v203, v225 op_sel_hi:[1,0,0]
	v_fma_mix_f32 v75, v145, v203, v225 op_sel:[1,0,0] op_sel_hi:[1,0,0]
	v_fma_mix_f32 v80, v146, v203, v225 op_sel_hi:[1,0,0]
	v_fma_mix_f32 v81, v146, v203, v225 op_sel:[1,0,0] op_sel_hi:[1,0,0]
	v_fma_mix_f32 v82, v147, v203, v225 op_sel_hi:[1,0,0]
	v_fma_mix_f32 v83, v147, v203, v225 op_sel:[1,0,0] op_sel_hi:[1,0,0]
	v_pk_fma_f32 v[20:21], v[72:73], v[168:169], v[20:21]
	v_pk_fma_f32 v[22:23], v[74:75], v[170:171], v[22:23]
	v_pk_fma_f32 v[16:17], v[80:81], v[172:173], v[16:17]
	v_pk_fma_f32 v[18:19], v[82:83], v[174:175], v[18:19]
	v_cvt_pk_f16_f32 v20, v20, v21
	v_cvt_pk_f16_f32 v21, v22, v23
	v_cvt_pk_f16_f32 v22, v16, v17
	v_cvt_pk_f16_f32 v23, v18, v19
	ds_write_b128 v235, v[20:23] offset:64
	v_fma_mix_f32 v210, v20, 1.0, v210 op_sel_hi:[1,0,0]
	v_fma_mix_f32 v211, v20, v20, v211 op_sel_hi:[1,1,0]
	v_fma_mix_f32 v210, v20, 1.0, v210 op_sel:[1,0,0] op_sel_hi:[1,0,0]
	v_fma_mix_f32 v211, v20, v20, v211 op_sel:[1,1,0] op_sel_hi:[1,1,0]
	v_fma_mix_f32 v210, v21, 1.0, v210 op_sel_hi:[1,0,0]
	v_fma_mix_f32 v211, v21, v21, v211 op_sel_hi:[1,1,0]
	v_fma_mix_f32 v210, v21, 1.0, v210 op_sel:[1,0,0] op_sel_hi:[1,0,0]
	v_fma_mix_f32 v211, v21, v21, v211 op_sel:[1,1,0] op_sel_hi:[1,1,0]
	v_fma_mix_f32 v210, v22, 1.0, v210 op_sel_hi:[1,0,0]
	v_fma_mix_f32 v211, v22, v22, v211 op_sel_hi:[1,1,0]
	v_fma_mix_f32 v210, v22, 1.0, v210 op_sel:[1,0,0] op_sel_hi:[1,0,0]
	v_fma_mix_f32 v211, v22, v22, v211 op_sel:[1,1,0] op_sel_hi:[1,1,0]
	v_fma_mix_f32 v210, v23, 1.0, v210 op_sel_hi:[1,0,0]
	v_fma_mix_f32 v211, v23, v23, v211 op_sel_hi:[1,1,0]
	v_fma_mix_f32 v210, v23, 1.0, v210 op_sel:[1,0,0] op_sel_hi:[1,0,0]
	v_fma_mix_f32 v211, v23, v23, v211 op_sel:[1,1,0] op_sel_hi:[1,1,0]
	ds_read_b128 v[240:243], v236
	ds_read_b128 v[96:99], v236 offset:1152
	v_mul_f32_e64 v225, -v204, v205
	s_waitcnt vmcnt(11)
	v_fma_mix_f32 v72, v132, v205, v225 op_sel_hi:[1,0,0]
	v_fma_mix_f32 v73, v132, v205, v225 op_sel:[1,0,0] op_sel_hi:[1,0,0]
	v_fma_mix_f32 v74, v133, v205, v225 op_sel_hi:[1,0,0]
	v_fma_mix_f32 v75, v133, v205, v225 op_sel:[1,0,0] op_sel_hi:[1,0,0]
	v_fma_mix_f32 v80, v134, v205, v225 op_sel_hi:[1,0,0]
	v_fma_mix_f32 v81, v134, v205, v225 op_sel:[1,0,0] op_sel_hi:[1,0,0]
	v_fma_mix_f32 v82, v135, v205, v225 op_sel_hi:[1,0,0]
	v_fma_mix_f32 v83, v135, v205, v225 op_sel:[1,0,0] op_sel_hi:[1,0,0]
	v_pk_fma_f32 v[12:13], v[72:73], v[160:161], v[12:13]
	v_pk_fma_f32 v[14:15], v[74:75], v[162:163], v[14:15]
	v_pk_fma_f32 v[8:9], v[80:81], v[164:165], v[8:9]
	v_pk_fma_f32 v[10:11], v[82:83], v[166:167], v[10:11]
	v_cvt_pk_f16_f32 v12, v12, v13
	v_cvt_pk_f16_f32 v13, v14, v15
	v_cvt_pk_f16_f32 v14, v8, v9
	v_cvt_pk_f16_f32 v15, v10, v11
	s_waitcnt lgkmcnt(0)
	v_add_u32_e32 v83, 0x3c000, v224
	buffer_store_dwordx4 v[240:243], v83, s[24:27], 0 offen nt
	v_add_u32_e32 v82, 0x3f000, v224
	buffer_store_dwordx4 v[96:99], v82, s[24:27], 0 offen nt
	ds_write_b128 v235, v[12:15]
	v_fma_mix_f32 v244, v12, 1.0, 0 op_sel_hi:[1,0,0]
	v_fma_mix_f32 v245, v12, v12, 0 op_sel_hi:[1,1,0]
	v_fma_mix_f32 v244, v12, 1.0, v244 op_sel:[1,0,0] op_sel_hi:[1,0,0]
	v_fma_mix_f32 v245, v12, v12, v245 op_sel:[1,1,0] op_sel_hi:[1,1,0]
	v_fma_mix_f32 v244, v13, 1.0, v244 op_sel_hi:[1,0,0]
	v_fma_mix_f32 v245, v13, v13, v245 op_sel_hi:[1,1,0]
	v_fma_mix_f32 v244, v13, 1.0, v244 op_sel:[1,0,0] op_sel_hi:[1,0,0]
	v_fma_mix_f32 v245, v13, v13, v245 op_sel:[1,1,0] op_sel_hi:[1,1,0]
	v_fma_mix_f32 v244, v14, 1.0, v244 op_sel_hi:[1,0,0]
	v_fma_mix_f32 v245, v14, v14, v245 op_sel_hi:[1,1,0]
	v_fma_mix_f32 v244, v14, 1.0, v244 op_sel:[1,0,0] op_sel_hi:[1,0,0]
	v_fma_mix_f32 v245, v14, v14, v245 op_sel:[1,1,0] op_sel_hi:[1,1,0]
	v_fma_mix_f32 v244, v15, 1.0, v244 op_sel_hi:[1,0,0]
	v_fma_mix_f32 v245, v15, v15, v245 op_sel_hi:[1,1,0]
	v_fma_mix_f32 v244, v15, 1.0, v244 op_sel:[1,0,0] op_sel_hi:[1,0,0]
	v_fma_mix_f32 v245, v15, v15, v245 op_sel:[1,1,0] op_sel_hi:[1,1,0]
	s_waitcnt vmcnt(12)
	v_fma_mix_f32 v72, v88, v205, v225 op_sel_hi:[1,0,0]
	v_fma_mix_f32 v73, v88, v205, v225 op_sel:[1,0,0] op_sel_hi:[1,0,0]
	v_fma_mix_f32 v74, v89, v205, v225 op_sel_hi:[1,0,0]
	v_fma_mix_f32 v75, v89, v205, v225 op_sel:[1,0,0] op_sel_hi:[1,0,0]
	v_fma_mix_f32 v80, v90, v205, v225 op_sel_hi:[1,0,0]
	v_fma_mix_f32 v81, v90, v205, v225 op_sel:[1,0,0] op_sel_hi:[1,0,0]
	v_fma_mix_f32 v82, v91, v205, v225 op_sel_hi:[1,0,0]
	v_fma_mix_f32 v83, v91, v205, v225 op_sel:[1,0,0] op_sel_hi:[1,0,0]
	v_pk_fma_f32 v[4:5], v[72:73], v[168:169], v[4:5]
	v_pk_fma_f32 v[6:7], v[74:75], v[170:171], v[6:7]
	v_pk_fma_f32 v[0:1], v[80:81], v[172:173], v[0:1]
	v_pk_fma_f32 v[2:3], v[82:83], v[174:175], v[2:3]
	v_cvt_pk_f16_f32 v4, v4, v5
	v_cvt_pk_f16_f32 v5, v6, v7
	v_cvt_pk_f16_f32 v6, v0, v1
	v_cvt_pk_f16_f32 v7, v2, v3
	ds_write_b128 v235, v[4:7] offset:64
	v_fma_mix_f32 v244, v4, 1.0, v244 op_sel_hi:[1,0,0]
	v_fma_mix_f32 v245, v4, v4, v245 op_sel_hi:[1,1,0]
	v_fma_mix_f32 v244, v4, 1.0, v244 op_sel:[1,0,0] op_sel_hi:[1,0,0]
	v_fma_mix_f32 v245, v4, v4, v245 op_sel:[1,1,0] op_sel_hi:[1,1,0]
	v_fma_mix_f32 v244, v5, 1.0, v244 op_sel_hi:[1,0,0]
	v_fma_mix_f32 v245, v5, v5, v245 op_sel_hi:[1,1,0]
	v_fma_mix_f32 v244, v5, 1.0, v244 op_sel:[1,0,0] op_sel_hi:[1,0,0]
	v_fma_mix_f32 v245, v5, v5, v245 op_sel:[1,1,0] op_sel_hi:[1,1,0]
	v_fma_mix_f32 v244, v6, 1.0, v244 op_sel_hi:[1,0,0]
	v_fma_mix_f32 v245, v6, v6, v245 op_sel_hi:[1,1,0]
	v_fma_mix_f32 v244, v6, 1.0, v244 op_sel:[1,0,0] op_sel_hi:[1,0,0]
	v_fma_mix_f32 v245, v6, v6, v245 op_sel:[1,1,0] op_sel_hi:[1,1,0]
	v_fma_mix_f32 v244, v7, 1.0, v244 op_sel_hi:[1,0,0]
	v_fma_mix_f32 v245, v7, v7, v245 op_sel_hi:[1,1,0]
	v_fma_mix_f32 v244, v7, 1.0, v244 op_sel:[1,0,0] op_sel_hi:[1,0,0]
	v_fma_mix_f32 v245, v7, v7, v245 op_sel:[1,1,0] op_sel_hi:[1,1,0]
	ds_read_b128 v[108:111], v236
	ds_read_b128 v[100:103], v236 offset:1152
	s_waitcnt lgkmcnt(0)
	v_add_u32_e32 v83, 0x42000, v224
	buffer_store_dwordx4 v[108:111], v83, s[24:27], 0 offen nt
	v_add_u32_e32 v82, 0x45000, v224
	buffer_store_dwordx4 v[100:103], v82, s[24:27], 0 offen nt
	v_xor_b32_e32 v246, 16, v234
	v_lshlrev_b32_e32 v246, 2, v246
	v_xor_b32_e32 v247, 32, v234
	v_lshlrev_b32_e32 v247, 2, v247
	ds_bpermute_b32 v92, v246, v206
	ds_bpermute_b32 v93, v246, v207
	ds_bpermute_b32 v94, v246, v140
	ds_bpermute_b32 v95, v246, v141
	ds_bpermute_b32 v120, v246, v142
	ds_bpermute_b32 v121, v246, v143
	ds_bpermute_b32 v122, v246, v216
	ds_bpermute_b32 v123, v246, v217
	s_waitcnt lgkmcnt(0)
	v_pk_add_f32 v[206:207], v[206:207], v[92:93]
	v_pk_add_f32 v[140:141], v[140:141], v[94:95]
	v_pk_add_f32 v[142:143], v[142:143], v[120:121]
	v_pk_add_f32 v[216:217], v[216:217], v[122:123]
	ds_bpermute_b32 v92, v246, v218
	ds_bpermute_b32 v93, v246, v219
	ds_bpermute_b32 v94, v246, v208
	ds_bpermute_b32 v95, v246, v209
	ds_bpermute_b32 v120, v246, v210
	ds_bpermute_b32 v121, v246, v211
	ds_bpermute_b32 v122, v246, v244
	ds_bpermute_b32 v123, v246, v245
	s_waitcnt lgkmcnt(0)
	v_pk_add_f32 v[218:219], v[218:219], v[92:93]
	v_pk_add_f32 v[208:209], v[208:209], v[94:95]
	v_pk_add_f32 v[210:211], v[210:211], v[120:121]
	v_pk_add_f32 v[244:245], v[244:245], v[122:123]
	ds_bpermute_b32 v92, v247, v206
	ds_bpermute_b32 v93, v247, v207
	ds_bpermute_b32 v94, v247, v140
	ds_bpermute_b32 v95, v247, v141
	ds_bpermute_b32 v120, v247, v142
	ds_bpermute_b32 v121, v247, v143
	ds_bpermute_b32 v122, v247, v216
	ds_bpermute_b32 v123, v247, v217
	s_waitcnt lgkmcnt(0)
	v_pk_add_f32 v[206:207], v[206:207], v[92:93]
	v_pk_add_f32 v[140:141], v[140:141], v[94:95]
	v_pk_add_f32 v[142:143], v[142:143], v[120:121]
	v_pk_add_f32 v[216:217], v[216:217], v[122:123]
	ds_bpermute_b32 v92, v247, v218
	ds_bpermute_b32 v93, v247, v219
	ds_bpermute_b32 v94, v247, v208
	ds_bpermute_b32 v95, v247, v209
	ds_bpermute_b32 v120, v247, v210
	ds_bpermute_b32 v121, v247, v211
	ds_bpermute_b32 v122, v247, v244
	ds_bpermute_b32 v123, v247, v245
	s_waitcnt lgkmcnt(0)
	v_pk_add_f32 v[218:219], v[218:219], v[92:93]
	v_pk_add_f32 v[208:209], v[208:209], v[94:95]
	v_pk_add_f32 v[210:211], v[210:211], v[120:121]
	v_pk_add_f32 v[244:245], v[244:245], v[122:123]
	s_mov_b64 exec, 0xffff
	global_store_dwordx2 v190, v[206:207], s[100:101] offset:0
	global_store_dwordx2 v190, v[140:141], s[100:101] offset:128
	global_store_dwordx2 v190, v[142:143], s[100:101] offset:256
	global_store_dwordx2 v190, v[216:217], s[100:101] offset:384
	global_store_dwordx2 v190, v[218:219], s[100:101] offset:1024
	global_store_dwordx2 v190, v[208:209], s[100:101] offset:1152
	global_store_dwordx2 v190, v[210:211], s[100:101] offset:1280
	global_store_dwordx2 v190, v[244:245], s[100:101] offset:1408
	s_mov_b64 exec, -1
	s_mov_b32 s83, s81
	s_mov_b32 s84, s82
	s_mov_b64 s[40:41], s[0:1]
	s_mov_b64 s[38:39], s[8:9]
	s_mov_b64 vcc, s[6:7]
	s_cbranch_vccz .LBB10_12
	s_waitcnt vmcnt(0)
	s_cmpk_gt_u32 s44, 0xff
	s_cbranch_scc1 .LBB10_31
	s_barrier

.LBB10_32:
	s_endpgm
	s_endpgm
	s_endpgm
	s_endpgm
	s_endpgm
	s_endpgm
	s_endpgm
	s_endpgm
	.section	.rodata,"a",@progbits
	.p2align	6, 0x0
